# baseline (speedup 1.0000x reference)
.LBB1_1:
	s_and_b32 s0, s29, 0x10000
	v_add_u32_e32 v211, s0, v209
	v_add_u32_e32 v242, s0, v210
	ds_read_b128 v[212:215], v242 offset:0
	ds_read_b128 v[216:219], v242 offset:0x800
	ds_read_b128 v[220:223], v242 offset:0x1000
	ds_read_b128 v[224:227], v242 offset:0x1800
	ds_read_b128 v[228:231], v211 offset:0
	ds_read_b128 v[232:235], v211 offset:0x800
	ds_read_b128 v[236:239], v211 offset:0x1000
	s_waitcnt lgkmcnt(2)
	v_mfma_f32_16x16x32_bf16 v[174:177], v[212:215], v[228:231], v[174:177]
	v_mfma_f32_16x16x32_bf16 v[170:173], v[216:219], v[228:231], v[170:173]
	v_mfma_f32_16x16x32_bf16 v[166:169], v[220:223], v[228:231], v[166:169]
	v_mfma_f32_16x16x32_bf16 v[162:165], v[224:227], v[228:231], v[162:165]
	ds_read_b128 v[228:231], v211 offset:0x1800
	s_waitcnt lgkmcnt(2)
	v_mfma_f32_16x16x32_bf16 v[158:161], v[212:215], v[232:235], v[158:161]
	v_mfma_f32_16x16x32_bf16 v[154:157], v[216:219], v[232:235], v[154:157]
	v_mfma_f32_16x16x32_bf16 v[150:153], v[220:223], v[232:235], v[150:153]
	v_mfma_f32_16x16x32_bf16 v[146:149], v[224:227], v[232:235], v[146:149]
	ds_read_b128 v[232:235], v211 offset:0x2000
	s_waitcnt lgkmcnt(2)
	v_mfma_f32_16x16x32_bf16 v[142:145], v[212:215], v[236:239], v[142:145]
	v_mfma_f32_16x16x32_bf16 v[138:141], v[216:219], v[236:239], v[138:141]
	v_mfma_f32_16x16x32_bf16 v[134:137], v[220:223], v[236:239], v[134:137]
	v_mfma_f32_16x16x32_bf16 v[130:133], v[224:227], v[236:239], v[130:133]
	ds_read_b128 v[236:239], v211 offset:0x2800
	s_waitcnt lgkmcnt(2)
	v_mfma_f32_16x16x32_bf16 v[126:129], v[212:215], v[228:231], v[126:129]
	v_mfma_f32_16x16x32_bf16 v[122:125], v[216:219], v[228:231], v[122:125]
	v_mfma_f32_16x16x32_bf16 v[118:121], v[220:223], v[228:231], v[118:121]
	v_mfma_f32_16x16x32_bf16 v[114:117], v[224:227], v[228:231], v[114:117]
	ds_read_b128 v[228:231], v211 offset:0x3000
	s_waitcnt lgkmcnt(2)
	v_mfma_f32_16x16x32_bf16 v[110:113], v[212:215], v[232:235], v[110:113]
	v_mfma_f32_16x16x32_bf16 v[106:109], v[216:219], v[232:235], v[106:109]
	v_mfma_f32_16x16x32_bf16 v[102:105], v[220:223], v[232:235], v[102:105]
	v_mfma_f32_16x16x32_bf16 v[98:101], v[224:227], v[232:235], v[98:101]
	ds_read_b128 v[232:235], v211 offset:0x3800
	s_waitcnt lgkmcnt(2)
	v_mfma_f32_16x16x32_bf16 v[94:97], v[212:215], v[236:239], v[94:97]
	v_mfma_f32_16x16x32_bf16 v[90:93], v[216:219], v[236:239], v[90:93]
	v_mfma_f32_16x16x32_bf16 v[86:89], v[220:223], v[236:239], v[86:89]
	v_mfma_f32_16x16x32_bf16 v[82:85], v[224:227], v[236:239], v[82:85]
	s_waitcnt lgkmcnt(1)
	v_mfma_f32_16x16x32_bf16 v[78:81], v[212:215], v[228:231], v[78:81]
	v_mfma_f32_16x16x32_bf16 v[74:77], v[216:219], v[228:231], v[74:77]
	v_mfma_f32_16x16x32_bf16 v[70:73], v[220:223], v[228:231], v[70:73]
	v_mfma_f32_16x16x32_bf16 v[66:69], v[224:227], v[228:231], v[66:69]
	s_waitcnt lgkmcnt(0)
	v_mfma_f32_16x16x32_bf16 v[62:65], v[212:215], v[232:235], v[62:65]
	v_mfma_f32_16x16x32_bf16 v[58:61], v[216:219], v[232:235], v[58:61]
	v_mfma_f32_16x16x32_bf16 v[54:57], v[220:223], v[232:235], v[54:57]
	v_mfma_f32_16x16x32_bf16 v[50:53], v[224:227], v[232:235], v[50:53]
	s_xor_b32 s0, s0, 0x10000
	s_and_b32 s1, s22, 0x3c0
	s_add_i32 s23, s0, 0
	s_lshl_b32 s0, s1, 2
	s_add_u32 s20, s25, s0
	s_waitcnt vmcnt(10)
	v_cvt_pk_bf16_f32 v46, v46, v47
	v_cvt_pk_bf16_f32 v47, v48, v49
	v_cvt_pk_bf16_f32 v48, v42, v43
	v_cvt_pk_bf16_f32 v49, v44, v45
	s_waitcnt vmcnt(8)
	v_cvt_pk_bf16_f32 v38, v38, v39
	v_cvt_pk_bf16_f32 v39, v40, v41
	v_cvt_pk_bf16_f32 v40, v34, v35
	v_add_u32_e32 v34, s23, v208
	s_addc_u32 s21, s26, 0
	s_lshl_b32 s0, s1, 1
	v_cvt_pk_bf16_f32 v41, v36, v37
	v_lshlrev_b32_e32 v182, 2, v178
	v_add_u32_e32 v35, s23, v205
	v_add_u32_e32 v36, s23, v206
	v_add_u32_e32 v37, s23, v207
	ds_write_b128 v34, v[46:49]
	ds_write_b128 v35, v[38:41]
	s_waitcnt vmcnt(7)
	ds_write_b128 v36, v[30:33] offset:32768
	s_waitcnt vmcnt(6)
	ds_write_b128 v37, v[26:29] offset:32768
	v_lshl_add_u64 v[26:27], s[20:21], 0, v[180:181]
	v_lshl_add_u64 v[28:29], s[20:21], 0, v[184:185]
	s_add_u32 s0, s27, s0
	v_lshl_add_u64 v[26:27], v[26:27], 0, v[182:183]
	v_lshl_add_u64 v[28:29], v[28:29], 0, v[182:183]
	s_addc_u32 s1, s28, 0
	v_lshlrev_b32_e32 v240, 1, v178
	v_mov_b32_e32 v241, v183
	global_load_dwordx4 v[42:45], v[26:27], off offset:16
	global_load_dwordx4 v[46:49], v[26:27], off
	global_load_dwordx4 v[34:37], v[28:29], off offset:16
	global_load_dwordx4 v[38:41], v[28:29], off
	v_lshl_add_u64 v[26:27], s[0:1], 0, v[186:187]
	v_lshl_add_u64 v[28:29], s[0:1], 0, v[188:189]
	v_lshl_add_u64 v[26:27], v[26:27], 0, v[240:241]
	v_lshl_add_u64 v[28:29], v[28:29], 0, v[240:241]
	global_load_dwordx4 v[30:33], v[26:27], off
	s_nop 0
	global_load_dwordx4 v[26:29], v[28:29], off
	ds_read_b128 v[212:215], v242 offset:0x400
	ds_read_b128 v[216:219], v242 offset:0xc00
	ds_read_b128 v[220:223], v242 offset:0x1400
	ds_read_b128 v[224:227], v242 offset:0x1c00
	ds_read_b128 v[228:231], v211 offset:0x400
	ds_read_b128 v[232:235], v211 offset:0xc00
	ds_read_b128 v[236:239], v211 offset:0x1400
	s_waitcnt lgkmcnt(2)
	v_mfma_f32_16x16x32_bf16 v[174:177], v[212:215], v[228:231], v[174:177]
	v_mfma_f32_16x16x32_bf16 v[170:173], v[216:219], v[228:231], v[170:173]
	v_mfma_f32_16x16x32_bf16 v[166:169], v[220:223], v[228:231], v[166:169]
	v_mfma_f32_16x16x32_bf16 v[162:165], v[224:227], v[228:231], v[162:165]
	ds_read_b128 v[228:231], v211 offset:0x1c00
	s_waitcnt lgkmcnt(2)
	v_mfma_f32_16x16x32_bf16 v[158:161], v[212:215], v[232:235], v[158:161]
	v_mfma_f32_16x16x32_bf16 v[154:157], v[216:219], v[232:235], v[154:157]
	v_mfma_f32_16x16x32_bf16 v[150:153], v[220:223], v[232:235], v[150:153]
	v_mfma_f32_16x16x32_bf16 v[146:149], v[224:227], v[232:235], v[146:149]
	ds_read_b128 v[232:235], v211 offset:0x2400
	s_waitcnt lgkmcnt(2)
	v_mfma_f32_16x16x32_bf16 v[142:145], v[212:215], v[236:239], v[142:145]
	v_mfma_f32_16x16x32_bf16 v[138:141], v[216:219], v[236:239], v[138:141]
	v_mfma_f32_16x16x32_bf16 v[134:137], v[220:223], v[236:239], v[134:137]
	v_mfma_f32_16x16x32_bf16 v[130:133], v[224:227], v[236:239], v[130:133]
	ds_read_b128 v[236:239], v211 offset:0x2c00
	s_waitcnt lgkmcnt(2)
	v_mfma_f32_16x16x32_bf16 v[126:129], v[212:215], v[228:231], v[126:129]
	v_mfma_f32_16x16x32_bf16 v[122:125], v[216:219], v[228:231], v[122:125]
	v_mfma_f32_16x16x32_bf16 v[118:121], v[220:223], v[228:231], v[118:121]
	v_mfma_f32_16x16x32_bf16 v[114:117], v[224:227], v[228:231], v[114:117]
	ds_read_b128 v[228:231], v211 offset:0x3400
	s_waitcnt lgkmcnt(2)
	v_mfma_f32_16x16x32_bf16 v[110:113], v[212:215], v[232:235], v[110:113]
	v_mfma_f32_16x16x32_bf16 v[106:109], v[216:219], v[232:235], v[106:109]
	v_mfma_f32_16x16x32_bf16 v[102:105], v[220:223], v[232:235], v[102:105]
	v_mfma_f32_16x16x32_bf16 v[98:101], v[224:227], v[232:235], v[98:101]
	ds_read_b128 v[232:235], v211 offset:0x3c00
	s_waitcnt lgkmcnt(2)
	v_mfma_f32_16x16x32_bf16 v[94:97], v[212:215], v[236:239], v[94:97]
	v_mfma_f32_16x16x32_bf16 v[90:93], v[216:219], v[236:239], v[90:93]
	v_mfma_f32_16x16x32_bf16 v[86:89], v[220:223], v[236:239], v[86:89]
	v_mfma_f32_16x16x32_bf16 v[82:85], v[224:227], v[236:239], v[82:85]
	s_waitcnt lgkmcnt(1)
	v_mfma_f32_16x16x32_bf16 v[78:81], v[212:215], v[228:231], v[78:81]
	v_mfma_f32_16x16x32_bf16 v[74:77], v[216:219], v[228:231], v[74:77]
	v_mfma_f32_16x16x32_bf16 v[70:73], v[220:223], v[228:231], v[70:73]
	v_mfma_f32_16x16x32_bf16 v[66:69], v[224:227], v[228:231], v[66:69]
	s_waitcnt lgkmcnt(0)
	v_mfma_f32_16x16x32_bf16 v[62:65], v[212:215], v[232:235], v[62:65]
	v_mfma_f32_16x16x32_bf16 v[58:61], v[216:219], v[232:235], v[58:61]
	v_mfma_f32_16x16x32_bf16 v[54:57], v[220:223], v[232:235], v[54:57]
	v_mfma_f32_16x16x32_bf16 v[50:53], v[224:227], v[232:235], v[50:53]
	s_waitcnt vmcnt(10)
	v_cvt_pk_bf16_f32 v22, v22, v23
	v_cvt_pk_bf16_f32 v23, v24, v25
	v_cvt_pk_bf16_f32 v24, v6, v7
	v_cvt_pk_bf16_f32 v25, v8, v9
	v_add_u32_e32 v6, s23, v204
	s_waitcnt vmcnt(9)
	v_cvt_pk_bf16_f32 v8, v2, v3
	v_add_u32_e32 v2, s23, v201
	ds_write_b128 v6, v[22:25]
	s_waitcnt vmcnt(8)
	v_cvt_pk_bf16_f32 v6, v10, v11
	v_cvt_pk_bf16_f32 v7, v12, v13
	v_cvt_pk_bf16_f32 v9, v4, v5
	ds_write_b128 v2, v[6:9]
	v_add_u32_e32 v2, s23, v202
	s_waitcnt vmcnt(7)
	ds_write_b128 v2, v[18:21] offset:32768
	v_add_u32_e32 v2, s23, v203
	s_waitcnt vmcnt(6)
	ds_write_b128 v2, v[14:17] offset:32768
	v_lshl_add_u64 v[2:3], s[20:21], 0, v[190:191]
	v_lshl_add_u64 v[2:3], v[2:3], 0, v[182:183]
	global_load_dwordx4 v[6:9], v[2:3], off offset:16
	global_load_dwordx4 v[22:25], v[2:3], off
	v_lshl_add_u64 v[2:3], s[20:21], 0, v[192:193]
	v_lshl_add_u64 v[14:15], s[0:1], 0, v[194:195]
	v_lshl_add_u64 v[16:17], s[0:1], 0, v[196:197]
	v_lshl_add_u64 v[10:11], v[2:3], 0, v[182:183]
	v_lshl_add_u64 v[14:15], v[14:15], 0, v[240:241]
	v_lshl_add_u64 v[16:17], v[16:17], 0, v[240:241]
	global_load_dwordx4 v[2:5], v[10:11], off offset:16
	s_nop 0
	global_load_dwordx4 v[10:13], v[10:11], off
	s_nop 0
	global_load_dwordx4 v[18:21], v[14:15], off
	s_nop 0
	global_load_dwordx4 v[14:17], v[16:17], off
	s_waitcnt lgkmcnt(0)
	s_add_i32 s22, s22, 64
	s_add_i32 s29, s29, 0x10000
	s_cmp_lg_u32 s29, 0xe0000
	s_barrier
	s_cbranch_scc1 .LBB1_1
	s_lshl_b64 s[0:1], s[18:19], 24
	ds_read_b128 v[180:183], v210 offset:0
	ds_read_b128 v[184:187], v210 offset:0x800
	ds_read_b128 v[188:191], v210 offset:0x1000
	ds_read_b128 v[192:195], v210 offset:0x1800
	ds_read_b128 v[212:215], v209 offset:0
	ds_read_b128 v[216:219], v209 offset:0x800
	ds_read_b128 v[220:223], v209 offset:0x1000
	s_waitcnt lgkmcnt(0)
	s_add_u32 s0, s10, s0
	s_addc_u32 s18, s11, s1
	s_lshl_b32 s19, s24, 1
	s_mov_b32 s1, 0
	s_add_u32 s0, s0, s19
	s_waitcnt lgkmcnt(2)
	s_addc_u32 s20, s18, 0
	v_mfma_f32_16x16x32_bf16 v[174:177], v[180:183], v[212:215], v[174:177]
	v_mfma_f32_16x16x32_bf16 v[170:173], v[184:187], v[212:215], v[170:173]
	v_mfma_f32_16x16x32_bf16 v[166:169], v[188:191], v[212:215], v[166:169]
	v_mfma_f32_16x16x32_bf16 v[162:165], v[192:195], v[212:215], v[162:165]
	ds_read_b128 v[212:215], v209 offset:0x1800
	s_waitcnt lgkmcnt(2)
	v_mfma_f32_16x16x32_bf16 v[158:161], v[180:183], v[216:219], v[158:161]
	v_mfma_f32_16x16x32_bf16 v[154:157], v[184:187], v[216:219], v[154:157]
	v_mfma_f32_16x16x32_bf16 v[150:153], v[188:191], v[216:219], v[150:153]
	v_mfma_f32_16x16x32_bf16 v[146:149], v[192:195], v[216:219], v[146:149]
	ds_read_b128 v[216:219], v209 offset:0x2000
	s_waitcnt lgkmcnt(2)
	v_mfma_f32_16x16x32_bf16 v[142:145], v[180:183], v[220:223], v[142:145]
	v_mfma_f32_16x16x32_bf16 v[138:141], v[184:187], v[220:223], v[138:141]
	v_mfma_f32_16x16x32_bf16 v[134:137], v[188:191], v[220:223], v[134:137]
	v_mfma_f32_16x16x32_bf16 v[130:133], v[192:195], v[220:223], v[130:133]
	ds_read_b128 v[220:223], v209 offset:0x2800
	s_waitcnt lgkmcnt(2)
	v_mfma_f32_16x16x32_bf16 v[126:129], v[180:183], v[212:215], v[126:129]
	v_mfma_f32_16x16x32_bf16 v[122:125], v[184:187], v[212:215], v[122:125]
	v_mfma_f32_16x16x32_bf16 v[118:121], v[188:191], v[212:215], v[118:121]
	v_mfma_f32_16x16x32_bf16 v[114:117], v[192:195], v[212:215], v[114:117]
	ds_read_b128 v[212:215], v209 offset:0x3000
	s_waitcnt lgkmcnt(2)
	v_mfma_f32_16x16x32_bf16 v[110:113], v[180:183], v[216:219], v[110:113]
	v_mfma_f32_16x16x32_bf16 v[106:109], v[184:187], v[216:219], v[106:109]
	v_mfma_f32_16x16x32_bf16 v[102:105], v[188:191], v[216:219], v[102:105]
	v_mfma_f32_16x16x32_bf16 v[98:101], v[192:195], v[216:219], v[98:101]
	ds_read_b128 v[216:219], v209 offset:0x3800
	s_waitcnt lgkmcnt(2)
	v_mfma_f32_16x16x32_bf16 v[94:97], v[180:183], v[220:223], v[94:97]
	v_mfma_f32_16x16x32_bf16 v[90:93], v[184:187], v[220:223], v[90:93]
	v_mfma_f32_16x16x32_bf16 v[86:89], v[188:191], v[220:223], v[86:89]
	v_mfma_f32_16x16x32_bf16 v[82:85], v[192:195], v[220:223], v[82:85]
	s_waitcnt lgkmcnt(1)
	v_mfma_f32_16x16x32_bf16 v[78:81], v[180:183], v[212:215], v[78:81]
	v_mfma_f32_16x16x32_bf16 v[74:77], v[184:187], v[212:215], v[74:77]
	v_mfma_f32_16x16x32_bf16 v[70:73], v[188:191], v[212:215], v[70:73]
	v_mfma_f32_16x16x32_bf16 v[66:69], v[192:195], v[212:215], v[66:69]
	s_waitcnt lgkmcnt(0)
	v_mfma_f32_16x16x32_bf16 v[62:65], v[180:183], v[216:219], v[62:65]
	v_mfma_f32_16x16x32_bf16 v[58:61], v[184:187], v[216:219], v[58:61]
	v_mfma_f32_16x16x32_bf16 v[54:57], v[188:191], v[216:219], v[54:57]
	v_mfma_f32_16x16x32_bf16 v[50:53], v[192:195], v[216:219], v[50:53]
	s_add_i32 s18, 0, 0x10000
	s_waitcnt vmcnt(10)
	v_cvt_pk_bf16_f32 v46, v46, v47
	v_cvt_pk_bf16_f32 v47, v48, v49
	v_cvt_pk_bf16_f32 v48, v42, v43
	v_add_u32_e32 v42, s18, v208
	s_waitcnt vmcnt(8)
	v_cvt_pk_bf16_f32 v38, v38, v39
	v_cvt_pk_bf16_f32 v39, v40, v41
	v_cvt_pk_bf16_f32 v40, v34, v35
	v_add_u32_e32 v34, s18, v205
	s_add_i32 s19, 0, 0x18000
	v_cvt_pk_bf16_f32 v49, v44, v45
	ds_write_b128 v42, v[46:49]
	v_cvt_pk_bf16_f32 v41, v36, v37
	ds_write_b128 v34, v[38:41]
	v_add_u32_e32 v34, s19, v206
	s_waitcnt vmcnt(7)
	ds_write_b128 v34, v[30:33]
	v_add_u32_e32 v30, s19, v207
	s_waitcnt vmcnt(6)
	ds_write_b128 v30, v[26:29]
	ds_read_b128 v[26:29], v210 offset:0x400
	ds_read_b128 v[30:33], v210 offset:0xc00
	ds_read_b128 v[34:37], v210 offset:0x1400
	ds_read_b128 v[38:41], v210 offset:0x1c00
	ds_read_b128 v[42:45], v209 offset:0x400
	ds_read_b128 v[46:49], v209 offset:0xc00
	ds_read_b128 v[180:183], v209 offset:0x1400
	s_waitcnt lgkmcnt(2)
	v_mfma_f32_16x16x32_bf16 v[174:177], v[26:29], v[42:45], v[174:177]
	v_mfma_f32_16x16x32_bf16 v[170:173], v[30:33], v[42:45], v[170:173]
	v_mfma_f32_16x16x32_bf16 v[166:169], v[34:37], v[42:45], v[166:169]
	v_mfma_f32_16x16x32_bf16 v[42:45], v[38:41], v[42:45], v[162:165]
	ds_read_b128 v[162:165], v209 offset:0x1c00
	s_waitcnt lgkmcnt(2)
	v_mfma_f32_16x16x32_bf16 v[158:161], v[26:29], v[46:49], v[158:161]
	v_mfma_f32_16x16x32_bf16 v[154:157], v[30:33], v[46:49], v[154:157]
	v_mfma_f32_16x16x32_bf16 v[150:153], v[34:37], v[46:49], v[150:153]
	v_mfma_f32_16x16x32_bf16 v[46:49], v[38:41], v[46:49], v[146:149]
	ds_read_b128 v[146:149], v209 offset:0x2400
	s_waitcnt lgkmcnt(2)
	v_mfma_f32_16x16x32_bf16 v[142:145], v[26:29], v[180:183], v[142:145]
	v_mfma_f32_16x16x32_bf16 v[138:141], v[30:33], v[180:183], v[138:141]
	v_mfma_f32_16x16x32_bf16 v[134:137], v[34:37], v[180:183], v[134:137]
	v_mfma_f32_16x16x32_bf16 v[130:133], v[38:41], v[180:183], v[130:133]
	ds_read_b128 v[180:183], v209 offset:0x2c00
	s_waitcnt lgkmcnt(2)
	v_mfma_f32_16x16x32_bf16 v[126:129], v[26:29], v[162:165], v[126:129]
	v_mfma_f32_16x16x32_bf16 v[122:125], v[30:33], v[162:165], v[122:125]
	v_mfma_f32_16x16x32_bf16 v[118:121], v[34:37], v[162:165], v[118:121]
	v_mfma_f32_16x16x32_bf16 v[114:117], v[38:41], v[162:165], v[114:117]
	ds_read_b128 v[162:165], v209 offset:0x3400
	s_waitcnt lgkmcnt(2)
	v_mfma_f32_16x16x32_bf16 v[110:113], v[26:29], v[146:149], v[110:113]
	v_mfma_f32_16x16x32_bf16 v[106:109], v[30:33], v[146:149], v[106:109]
	v_mfma_f32_16x16x32_bf16 v[102:105], v[34:37], v[146:149], v[102:105]
	v_mfma_f32_16x16x32_bf16 v[98:101], v[38:41], v[146:149], v[98:101]
	ds_read_b128 v[146:149], v209 offset:0x3c00
	s_waitcnt lgkmcnt(2)
	v_mfma_f32_16x16x32_bf16 v[94:97], v[26:29], v[180:183], v[94:97]
	v_mfma_f32_16x16x32_bf16 v[90:93], v[30:33], v[180:183], v[90:93]
	v_mfma_f32_16x16x32_bf16 v[86:89], v[34:37], v[180:183], v[86:89]
	v_mfma_f32_16x16x32_bf16 v[82:85], v[38:41], v[180:183], v[82:85]
	s_waitcnt lgkmcnt(1)
	v_mfma_f32_16x16x32_bf16 v[78:81], v[26:29], v[162:165], v[78:81]
	v_mfma_f32_16x16x32_bf16 v[74:77], v[30:33], v[162:165], v[74:77]
	v_mfma_f32_16x16x32_bf16 v[70:73], v[34:37], v[162:165], v[70:73]
	v_mfma_f32_16x16x32_bf16 v[66:69], v[38:41], v[162:165], v[66:69]
	s_waitcnt lgkmcnt(0)
	v_mfma_f32_16x16x32_bf16 v[26:29], v[26:29], v[146:149], v[62:65]
	v_mfma_f32_16x16x32_bf16 v[30:33], v[30:33], v[146:149], v[58:61]
	v_mfma_f32_16x16x32_bf16 v[34:37], v[34:37], v[146:149], v[54:57]
	v_mfma_f32_16x16x32_bf16 v[38:41], v[38:41], v[146:149], v[50:53]
	s_waitcnt vmcnt(4)
	v_cvt_pk_bf16_f32 v22, v22, v23
	v_cvt_pk_bf16_f32 v23, v24, v25
	v_cvt_pk_bf16_f32 v24, v6, v7
	v_cvt_pk_bf16_f32 v25, v8, v9
	v_add_u32_e32 v6, s18, v204
	s_waitcnt vmcnt(3)
	v_cvt_pk_bf16_f32 v8, v2, v3
	v_add_u32_e32 v2, s18, v201
	ds_write_b128 v6, v[22:25]
	s_waitcnt vmcnt(2)
	v_cvt_pk_bf16_f32 v6, v10, v11
	v_cvt_pk_bf16_f32 v7, v12, v13
	v_cvt_pk_bf16_f32 v9, v4, v5
	ds_write_b128 v2, v[6:9]
	v_add_u32_e32 v2, s19, v202
	s_waitcnt vmcnt(1)
	ds_write_b128 v2, v[18:21]
	v_add_u32_e32 v2, s19, v203
	s_waitcnt vmcnt(0)
	ds_write_b128 v2, v[14:17]
	s_waitcnt lgkmcnt(0)
	s_barrier
	v_add_u32_e32 v178, 0x10000, v209
	v_add_u32_e32 v196, 0x10000, v210
	ds_read_b128 v[2:5], v196 offset:0
	ds_read_b128 v[6:9], v196 offset:0x800
	ds_read_b128 v[10:13], v196 offset:0x1000
	ds_read_b128 v[14:17], v196 offset:0x1800
	ds_read_b128 v[18:21], v178 offset:0
	s_and_b64 s[16:17], s[16:17], exec
	ds_read_b128 v[22:25], v178 offset:0x800
	ds_read_b128 v[50:53], v178 offset:0x1000
	s_waitcnt lgkmcnt(2)
	s_cselect_b32 s5, s5, s7
	s_cselect_b32 s4, s4, s6
	s_lshl_b32 s6, s3, 10
	v_mfma_f32_16x16x32_bf16 v[54:57], v[2:5], v[18:21], v[174:177]
	s_add_u32 s6, s4, s6
	s_addc_u32 s7, s5, 0
	s_lshl_b32 s3, s3, 9
	v_mfma_f32_16x16x32_bf16 v[58:61], v[6:9], v[18:21], v[170:173]
	s_add_u32 s4, s0, s3
	s_addc_u32 s5, s20, 0
	v_mfma_f32_16x16x32_bf16 v[62:65], v[10:13], v[18:21], v[166:169]
	v_mfma_f32_16x16x32_bf16 v[18:21], v[14:17], v[18:21], v[42:45]
	ds_read_b128 v[42:45], v178 offset:0x1800
	s_waitcnt lgkmcnt(2)
	v_mfma_f32_16x16x32_bf16 v[146:149], v[2:5], v[22:25], v[158:161]
	v_mfma_f32_16x16x32_bf16 v[154:157], v[6:9], v[22:25], v[154:157]
	v_mfma_f32_16x16x32_bf16 v[150:153], v[10:13], v[22:25], v[150:153]
	v_mfma_f32_16x16x32_bf16 v[22:25], v[14:17], v[22:25], v[46:49]
	ds_read_b128 v[46:49], v178 offset:0x2000
	s_waitcnt lgkmcnt(2)
	v_mfma_f32_16x16x32_bf16 v[142:145], v[2:5], v[50:53], v[142:145]
	v_mfma_f32_16x16x32_bf16 v[138:141], v[6:9], v[50:53], v[138:141]
	v_mfma_f32_16x16x32_bf16 v[134:137], v[10:13], v[50:53], v[134:137]
	v_mfma_f32_16x16x32_bf16 v[50:53], v[14:17], v[50:53], v[130:133]
	ds_read_b128 v[130:133], v178 offset:0x2800
	s_waitcnt lgkmcnt(2)
	v_mfma_f32_16x16x32_bf16 v[126:129], v[2:5], v[42:45], v[126:129]
	v_mfma_f32_16x16x32_bf16 v[122:125], v[6:9], v[42:45], v[122:125]
	v_mfma_f32_16x16x32_bf16 v[118:121], v[10:13], v[42:45], v[118:121]
	v_mfma_f32_16x16x32_bf16 v[42:45], v[14:17], v[42:45], v[114:117]
	ds_read_b128 v[114:117], v178 offset:0x3000
	s_waitcnt lgkmcnt(2)
	v_mfma_f32_16x16x32_bf16 v[110:113], v[2:5], v[46:49], v[110:113]
	v_mfma_f32_16x16x32_bf16 v[106:109], v[6:9], v[46:49], v[106:109]
	v_mfma_f32_16x16x32_bf16 v[102:105], v[10:13], v[46:49], v[102:105]
	v_mfma_f32_16x16x32_bf16 v[98:101], v[14:17], v[46:49], v[98:101]
	ds_read_b128 v[46:49], v178 offset:0x3800
	s_waitcnt lgkmcnt(2)
	v_mfma_f32_16x16x32_bf16 v[158:161], v[2:5], v[130:133], v[94:97]
	v_mfma_f32_16x16x32_bf16 v[162:165], v[6:9], v[130:133], v[90:93]
	v_mfma_f32_16x16x32_bf16 v[166:169], v[10:13], v[130:133], v[86:89]
	v_mfma_f32_16x16x32_bf16 v[130:133], v[14:17], v[130:133], v[82:85]
	s_waitcnt lgkmcnt(1)
	v_mfma_f32_16x16x32_bf16 v[66:69], v[14:17], v[114:117], v[66:69]
	v_mfma_f32_16x16x32_bf16 v[170:173], v[2:5], v[114:117], v[78:81]
	v_mfma_f32_16x16x32_bf16 v[174:177], v[6:9], v[114:117], v[74:77]
	v_mfma_f32_16x16x32_bf16 v[180:183], v[10:13], v[114:117], v[70:73]
	s_waitcnt lgkmcnt(0)
	v_mfma_f32_16x16x32_bf16 v[2:5], v[2:5], v[46:49], v[26:29]
	v_mfma_f32_16x16x32_bf16 v[114:117], v[6:9], v[46:49], v[30:33]
	v_mfma_f32_16x16x32_bf16 v[34:37], v[10:13], v[46:49], v[34:37]
	v_mfma_f32_16x16x32_bf16 v[184:187], v[14:17], v[46:49], v[38:41]
	ds_read_b128 v[188:191], v196 offset:0x400
	ds_read_b128 v[192:195], v196 offset:0xc00
	ds_read_b128 v[202:205], v196 offset:0x1400
	ds_read_b128 v[206:209], v196 offset:0x1c00
	ds_read_b128 v[6:9], v178 offset:0x400
	ds_read_b128 v[10:13], v178 offset:0xc00
	ds_read_b128 v[14:17], v178 offset:0x1400
	s_waitcnt lgkmcnt(2)
	v_mfma_f32_16x16x32_bf16 v[94:97], v[192:195], v[6:9], v[58:61]
	v_mfma_f32_16x16x32_bf16 v[62:65], v[202:205], v[6:9], v[62:65]
	v_mfma_f32_16x16x32_bf16 v[30:33], v[206:209], v[6:9], v[18:21]
	v_mfma_f32_16x16x32_bf16 v[210:213], v[188:191], v[6:9], v[54:57]
	ds_read_b128 v[6:9], v178 offset:0x1c00
	s_waitcnt lgkmcnt(2)
	v_mfma_f32_16x16x32_bf16 v[90:93], v[192:195], v[10:13], v[154:157]
	v_mfma_f32_16x16x32_bf16 v[58:61], v[202:205], v[10:13], v[150:153]
	v_mfma_f32_16x16x32_bf16 v[26:29], v[206:209], v[10:13], v[22:25]
	v_mfma_f32_16x16x32_bf16 v[146:149], v[188:191], v[10:13], v[146:149]
	ds_read_b128 v[10:13], v178 offset:0x2400
	s_waitcnt lgkmcnt(2)
	v_mfma_f32_16x16x32_bf16 v[86:89], v[192:195], v[14:17], v[138:141]
	v_mfma_f32_16x16x32_bf16 v[54:57], v[202:205], v[14:17], v[134:137]
	v_mfma_f32_16x16x32_bf16 v[22:25], v[206:209], v[14:17], v[50:53]
	v_mfma_f32_16x16x32_bf16 v[142:145], v[188:191], v[14:17], v[142:145]
	ds_read_b128 v[38:41], v178 offset:0x2c00
	s_waitcnt lgkmcnt(2)
	v_mfma_f32_16x16x32_bf16 v[126:129], v[188:191], v[6:9], v[126:129]
	v_mfma_f32_16x16x32_bf16 v[82:85], v[192:195], v[6:9], v[122:125]
	v_mfma_f32_16x16x32_bf16 v[50:53], v[202:205], v[6:9], v[118:121]
	v_mfma_f32_16x16x32_bf16 v[18:21], v[206:209], v[6:9], v[42:45]
	ds_read_b128 v[6:9], v178 offset:0x3400
	s_waitcnt lgkmcnt(2)
	v_mfma_f32_16x16x32_bf16 v[110:113], v[188:191], v[10:13], v[110:113]
	v_mfma_f32_16x16x32_bf16 v[78:81], v[192:195], v[10:13], v[106:109]
	v_mfma_f32_16x16x32_bf16 v[46:49], v[202:205], v[10:13], v[102:105]
	v_mfma_f32_16x16x32_bf16 v[14:17], v[206:209], v[10:13], v[98:101]
	ds_read_b128 v[98:101], v178 offset:0x3c00
	s_waitcnt lgkmcnt(2)
	v_mfma_f32_16x16x32_bf16 v[106:109], v[188:191], v[38:41], v[158:161]
	v_mfma_f32_16x16x32_bf16 v[74:77], v[192:195], v[38:41], v[162:165]
	v_mfma_f32_16x16x32_bf16 v[42:45], v[202:205], v[38:41], v[166:169]
	v_mfma_f32_16x16x32_bf16 v[10:13], v[206:209], v[38:41], v[130:133]
	s_waitcnt lgkmcnt(1)
	v_mfma_f32_16x16x32_bf16 v[118:121], v[188:191], v[6:9], v[170:173]
	v_mfma_f32_16x16x32_bf16 v[70:73], v[192:195], v[6:9], v[174:177]
	v_mfma_f32_16x16x32_bf16 v[38:41], v[202:205], v[6:9], v[180:183]
	v_mfma_f32_16x16x32_bf16 v[6:9], v[206:209], v[6:9], v[66:69]
	s_waitcnt lgkmcnt(0)
	v_mfma_f32_16x16x32_bf16 v[122:125], v[188:191], v[98:101], v[2:5]
	v_mfma_f32_16x16x32_bf16 v[66:69], v[192:195], v[98:101], v[114:117]
	v_mfma_f32_16x16x32_bf16 v[34:37], v[202:205], v[98:101], v[34:37]
	v_mfma_f32_16x16x32_bf16 v[2:5], v[206:209], v[98:101], v[184:187]
	v_lshrrev_b32_e32 v98, 2, v199
	v_and_b32_e32 v98, 12, v98
	v_lshl_or_b32 v104, v200, 6, v98
	v_lshlrev_b32_e32 v105, 2, v104
	s_waitcnt lgkmcnt(0)
	s_barrier
	global_load_dwordx4 v[114:117], v105, s[6:7]
	v_lshrrev_b32_e32 v98, 1, v199
	v_lshlrev_b32_e32 v99, 16, v198
	v_lshlrev_b32_e32 v100, 9, v179
	v_and_b32_e32 v102, 8, v98
	v_lshrrev_b32_e32 v98, 3, v104
	v_add3_u32 v103, 0, v99, v100
	v_xor_b32_e32 v130, v98, v179
	v_bitop3_b32 v131, v98, v179, 16 bitop3:0x1e
	global_load_dwordx4 v[98:101], v105, s[6:7] offset:64
	v_lshlrev_b32_e32 v130, 4, v130
	v_lshlrev_b32_e32 v131, 4, v131
	v_add3_u32 v130, v103, v130, v102
	v_add3_u32 v131, v103, v131, v102
	s_movk_i32 s0, 0x200
	s_waitcnt vmcnt(1)
	v_add_f32_e32 v132, v210, v114
	v_add_f32_e32 v133, v211, v115
	v_add_f32_e32 v134, v212, v116
	v_add_f32_e32 v135, v213, v117
	v_add_f32_e32 v140, v142, v114
	v_add_f32_e32 v141, v143, v115
	v_add_f32_e32 v142, v144, v116
	v_add_f32_e32 v143, v145, v117
	v_add_f32_e32 v110, v110, v114
	v_add_f32_e32 v111, v111, v115
	v_add_f32_e32 v106, v106, v114
	v_add_f32_e32 v107, v107, v115
	v_add_f32_e32 v136, v146, v114
	v_add_f32_e32 v137, v147, v115
	v_add_f32_e32 v138, v148, v116
	v_add_f32_e32 v139, v149, v117
	v_add_f32_e32 v126, v126, v114
	v_add_f32_e32 v127, v127, v115
	v_add_f32_e32 v128, v128, v116
	v_add_f32_e32 v129, v129, v117
	v_add_f32_e32 v112, v112, v116
	v_add_f32_e32 v113, v113, v117
	v_add_f32_e32 v108, v108, v116
	v_add_f32_e32 v109, v109, v117
	v_max_f32_e32 v132, 0, v132
	v_max_f32_e32 v133, 0, v133
	v_max_f32_e32 v134, 0, v134
	v_max_f32_e32 v135, 0, v135
	v_max_f32_e32 v140, 0, v140
	v_max_f32_e32 v141, 0, v141
	v_max_f32_e32 v142, 0, v142
	v_max_f32_e32 v143, 0, v143
	v_max_f32_e32 v144, 0, v110
	v_max_f32_e32 v145, 0, v111
	v_max_f32_e32 v148, 0, v106
	v_max_f32_e32 v149, 0, v107
	v_cvt_pk_bf16_f32 v106, v132, v133
	v_cvt_pk_bf16_f32 v107, v134, v135
	v_cvt_pk_bf16_f32 v110, v140, v141
	v_cvt_pk_bf16_f32 v111, v142, v143
	v_add_f32_e32 v118, v118, v114
	v_add_f32_e32 v119, v119, v115
	v_max_f32_e32 v136, 0, v136
	v_max_f32_e32 v137, 0, v137
	v_max_f32_e32 v138, 0, v138
	v_max_f32_e32 v139, 0, v139
	v_max_f32_e32 v126, 0, v126
	v_max_f32_e32 v127, 0, v127
	v_max_f32_e32 v128, 0, v128
	v_max_f32_e32 v129, 0, v129
	v_max_f32_e32 v146, 0, v112
	v_max_f32_e32 v147, 0, v113
	v_max_f32_e32 v150, 0, v108
	v_max_f32_e32 v151, 0, v109
	v_cvt_pk_bf16_f32 v108, v136, v137
	v_cvt_pk_bf16_f32 v109, v138, v139
	v_cvt_pk_bf16_f32 v112, v126, v127
	v_cvt_pk_bf16_f32 v113, v128, v129
	ds_write2st64_b64 v130, v[106:107], v[110:111] offset1:32
	ds_write2st64_b64 v131, v[108:109], v[112:113] offset0:16 offset1:48
	v_add_f32_e32 v106, v121, v117
	v_add_f32_e32 v120, v120, v116
	v_max_f32_e32 v152, 0, v118
	v_max_f32_e32 v153, 0, v119
	v_max_f32_e32 v107, 0, v106
	v_cvt_pk_bf16_f32 v106, v152, v153
	v_max_f32_e32 v120, 0, v120
	v_cvt_pk_bf16_f32 v118, v144, v145
	v_cvt_pk_bf16_f32 v119, v146, v147
	v_cvt_pk_bf16_f32 v107, v120, v107
	ds_write2st64_b64 v130, v[118:119], v[106:107] offset0:64 offset1:96
	v_add_f32_e32 v106, v122, v114
	v_max_f32_e32 v106, 0, v106
	v_add_f32_e32 v107, v123, v115
	v_max_f32_e32 v107, 0, v107
	v_add_f32_e32 v108, v124, v116
	v_add_f32_e32 v109, v125, v117
	v_cvt_pk_bf16_f32 v106, v106, v107
	v_cvt_pk_bf16_f32 v126, v148, v149
	v_cvt_pk_bf16_f32 v127, v150, v151
	v_max_f32_e32 v108, 0, v108
	v_max_f32_e32 v109, 0, v109
	v_cvt_pk_bf16_f32 v107, v108, v109
	ds_write2st64_b64 v131, v[126:127], v[106:107] offset0:80 offset1:112
	v_or_b32_e32 v106, 16, v104
	s_waitcnt vmcnt(0)
	v_add_f32_e32 v94, v94, v98
	v_add_f32_e32 v95, v95, v99
	v_add_f32_e32 v96, v96, v100
	v_lshrrev_b32_e32 v106, 3, v106
	v_max_f32_e32 v94, 0, v94
	v_max_f32_e32 v95, 0, v95
	v_max_f32_e32 v96, 0, v96
	v_add_f32_e32 v97, v97, v101
	v_max_f32_e32 v97, 0, v97
	v_cvt_pk_bf16_f32 v94, v94, v95
	v_cvt_pk_bf16_f32 v95, v96, v97
	v_xor_b32_e32 v96, v106, v179
	v_lshlrev_b32_e32 v96, 4, v96
	v_add3_u32 v107, v103, v96, v102
	v_add_f32_e32 v90, v90, v98
	v_add_f32_e32 v91, v91, v99
	v_add_f32_e32 v92, v92, v100
	ds_write_b64 v107, v[94:95]
	v_max_f32_e32 v90, 0, v90
	v_max_f32_e32 v91, 0, v91
	global_load_dwordx4 v[94:97], v105, s[6:7] offset:128
	v_max_f32_e32 v92, 0, v92
	v_add_f32_e32 v93, v93, v101
	v_max_f32_e32 v93, 0, v93
	v_cvt_pk_bf16_f32 v90, v90, v91
	v_cvt_pk_bf16_f32 v91, v92, v93
	v_bitop3_b32 v92, v106, v179, 16 bitop3:0x1e
	v_add_f32_e32 v66, v66, v98
	v_lshlrev_b32_e32 v92, 4, v92
	v_add_f32_e32 v86, v86, v98
	v_add_f32_e32 v87, v87, v99
	v_add_f32_e32 v82, v82, v98
	v_add_f32_e32 v83, v83, v99
	v_add_f32_e32 v78, v78, v98
	v_add_f32_e32 v79, v79, v99
	v_add_f32_e32 v74, v74, v98
	v_add_f32_e32 v75, v75, v99
	v_add_f32_e32 v70, v70, v98
	v_add_f32_e32 v71, v71, v99
	v_max_f32_e32 v66, 0, v66
	v_add_f32_e32 v67, v67, v99
	v_add3_u32 v92, v103, v92, v102
	v_max_f32_e32 v86, 0, v86
	v_max_f32_e32 v87, 0, v87
	v_add_f32_e32 v88, v88, v100
	v_add_f32_e32 v89, v89, v101
	v_max_f32_e32 v82, 0, v82
	v_max_f32_e32 v83, 0, v83
	v_add_f32_e32 v84, v84, v100
	v_add_f32_e32 v85, v85, v101
	v_max_f32_e32 v78, 0, v78
	v_max_f32_e32 v79, 0, v79
	v_add_f32_e32 v80, v80, v100
	v_add_f32_e32 v81, v81, v101
	v_max_f32_e32 v74, 0, v74
	v_max_f32_e32 v75, 0, v75
	v_add_f32_e32 v76, v76, v100
	v_add_f32_e32 v77, v77, v101
	v_max_f32_e32 v70, 0, v70
	v_max_f32_e32 v71, 0, v71
	v_add_f32_e32 v72, v72, v100
	v_add_f32_e32 v73, v73, v101
	v_max_f32_e32 v67, 0, v67
	v_add_f32_e32 v68, v68, v100
	v_add_f32_e32 v69, v69, v101
	v_cvt_pk_bf16_f32 v66, v66, v67
	ds_write_b64 v92, v[90:91] offset:8192
	v_max_f32_e32 v88, 0, v88
	v_max_f32_e32 v89, 0, v89
	v_cvt_pk_bf16_f32 v86, v86, v87
	v_cvt_pk_bf16_f32 v87, v88, v89
	ds_write_b64 v107, v[86:87] offset:16384
	v_max_f32_e32 v84, 0, v84
	v_max_f32_e32 v85, 0, v85
	v_cvt_pk_bf16_f32 v82, v82, v83
	v_cvt_pk_bf16_f32 v83, v84, v85
	ds_write_b64 v92, v[82:83] offset:24576
	v_max_f32_e32 v80, 0, v80
	v_max_f32_e32 v81, 0, v81
	v_cvt_pk_bf16_f32 v78, v78, v79
	v_cvt_pk_bf16_f32 v79, v80, v81
	ds_write_b64 v107, v[78:79] offset:32768
	v_max_f32_e32 v76, 0, v76
	v_max_f32_e32 v77, 0, v77
	v_cvt_pk_bf16_f32 v74, v74, v75
	v_cvt_pk_bf16_f32 v75, v76, v77
	ds_write_b64 v92, v[74:75] offset:40960
	v_max_f32_e32 v72, 0, v72
	v_max_f32_e32 v73, 0, v73
	v_cvt_pk_bf16_f32 v70, v70, v71
	v_cvt_pk_bf16_f32 v71, v72, v73
	ds_write_b64 v107, v[70:71] offset:49152
	v_max_f32_e32 v68, 0, v68
	v_max_f32_e32 v69, 0, v69
	v_cvt_pk_bf16_f32 v67, v68, v69
	ds_write_b64 v92, v[66:67] offset:57344
	v_or_b32_e32 v66, 32, v104
	v_lshrrev_b32_e32 v70, 3, v66
	global_load_dwordx4 v[66:69], v105, s[6:7] offset:192
	s_waitcnt vmcnt(1)
	v_add_f32_e32 v62, v62, v94
	v_add_f32_e32 v63, v63, v95
	v_add_f32_e32 v64, v64, v96
	v_add_f32_e32 v58, v58, v94
	v_add_f32_e32 v59, v59, v95
	v_add_f32_e32 v60, v60, v96
	v_max_f32_e32 v62, 0, v62
	v_max_f32_e32 v63, 0, v63
	v_max_f32_e32 v64, 0, v64
	v_add_f32_e32 v65, v65, v97
	v_max_f32_e32 v58, 0, v58
	v_max_f32_e32 v59, 0, v59
	v_max_f32_e32 v60, 0, v60
	v_add_f32_e32 v61, v61, v97
	v_max_f32_e32 v65, 0, v65
	v_cvt_pk_bf16_f32 v62, v62, v63
	v_cvt_pk_bf16_f32 v63, v64, v65
	v_xor_b32_e32 v64, v70, v179
	v_max_f32_e32 v61, 0, v61
	v_cvt_pk_bf16_f32 v58, v58, v59
	v_cvt_pk_bf16_f32 v59, v60, v61
	v_bitop3_b32 v60, v70, v179, 16 bitop3:0x1e
	v_add_f32_e32 v34, v34, v94
	v_lshlrev_b32_e32 v64, 4, v64
	v_lshlrev_b32_e32 v60, 4, v60
	v_add_f32_e32 v54, v54, v94
	v_add_f32_e32 v55, v55, v95
	v_add_f32_e32 v50, v50, v94
	v_add_f32_e32 v51, v51, v95
	v_add_f32_e32 v46, v46, v94
	v_add_f32_e32 v47, v47, v95
	v_add_f32_e32 v42, v42, v94
	v_add_f32_e32 v43, v43, v95
	v_add_f32_e32 v38, v38, v94
	v_add_f32_e32 v39, v39, v95
	v_max_f32_e32 v34, 0, v34
	v_add_f32_e32 v35, v35, v95
	v_add3_u32 v64, v103, v64, v102
	v_add3_u32 v60, v103, v60, v102
	v_max_f32_e32 v54, 0, v54
	v_max_f32_e32 v55, 0, v55
	v_add_f32_e32 v56, v56, v96
	v_add_f32_e32 v57, v57, v97
	v_max_f32_e32 v50, 0, v50
	v_max_f32_e32 v51, 0, v51
	v_add_f32_e32 v52, v52, v96
	v_add_f32_e32 v53, v53, v97
	v_max_f32_e32 v46, 0, v46
	v_max_f32_e32 v47, 0, v47
	v_add_f32_e32 v48, v48, v96
	v_add_f32_e32 v49, v49, v97
	v_max_f32_e32 v42, 0, v42
	v_max_f32_e32 v43, 0, v43
	v_add_f32_e32 v44, v44, v96
	v_add_f32_e32 v45, v45, v97
	v_max_f32_e32 v38, 0, v38
	v_max_f32_e32 v39, 0, v39
	v_add_f32_e32 v40, v40, v96
	v_add_f32_e32 v41, v41, v97
	v_max_f32_e32 v35, 0, v35
	v_add_f32_e32 v36, v36, v96
	v_add_f32_e32 v37, v37, v97
	v_cvt_pk_bf16_f32 v34, v34, v35
	ds_write_b64 v64, v[62:63]
	ds_write_b64 v60, v[58:59] offset:8192
	v_max_f32_e32 v56, 0, v56
	v_max_f32_e32 v57, 0, v57
	v_cvt_pk_bf16_f32 v54, v54, v55
	v_cvt_pk_bf16_f32 v55, v56, v57
	ds_write_b64 v64, v[54:55] offset:16384
	v_max_f32_e32 v52, 0, v52
	v_max_f32_e32 v53, 0, v53
	v_cvt_pk_bf16_f32 v50, v50, v51
	v_cvt_pk_bf16_f32 v51, v52, v53
	ds_write_b64 v60, v[50:51] offset:24576
	v_max_f32_e32 v48, 0, v48
	v_max_f32_e32 v49, 0, v49
	v_cvt_pk_bf16_f32 v46, v46, v47
	v_cvt_pk_bf16_f32 v47, v48, v49
	ds_write_b64 v64, v[46:47] offset:32768
	v_max_f32_e32 v44, 0, v44
	v_max_f32_e32 v45, 0, v45
	v_cvt_pk_bf16_f32 v42, v42, v43
	v_cvt_pk_bf16_f32 v43, v44, v45
	ds_write_b64 v60, v[42:43] offset:40960
	v_max_f32_e32 v40, 0, v40
	v_max_f32_e32 v41, 0, v41
	v_cvt_pk_bf16_f32 v38, v38, v39
	v_cvt_pk_bf16_f32 v39, v40, v41
	ds_write_b64 v64, v[38:39] offset:49152
	v_max_f32_e32 v36, 0, v36
	v_max_f32_e32 v37, 0, v37
	v_cvt_pk_bf16_f32 v35, v36, v37
	ds_write_b64 v60, v[34:35] offset:57344
	v_or_b32_e32 v34, 48, v104
	s_waitcnt vmcnt(0)
	v_add_f32_e32 v30, v30, v66
	v_add_f32_e32 v31, v31, v67
	v_add_f32_e32 v32, v32, v68
	v_add_f32_e32 v26, v26, v66
	v_add_f32_e32 v27, v27, v67
	v_add_f32_e32 v28, v28, v68
	v_lshrrev_b32_e32 v34, 3, v34
	v_max_f32_e32 v30, 0, v30
	v_max_f32_e32 v31, 0, v31
	v_max_f32_e32 v32, 0, v32
	v_add_f32_e32 v33, v33, v69
	v_max_f32_e32 v26, 0, v26
	v_max_f32_e32 v27, 0, v27
	v_max_f32_e32 v28, 0, v28
	v_add_f32_e32 v29, v29, v69
	v_max_f32_e32 v33, 0, v33
	v_cvt_pk_bf16_f32 v30, v30, v31
	v_cvt_pk_bf16_f32 v31, v32, v33
	v_xor_b32_e32 v32, v34, v179
	v_max_f32_e32 v29, 0, v29
	v_cvt_pk_bf16_f32 v26, v26, v27
	v_cvt_pk_bf16_f32 v27, v28, v29
	v_bitop3_b32 v28, v34, v179, 16 bitop3:0x1e
	v_add_f32_e32 v2, v2, v66
	v_lshlrev_b32_e32 v32, 4, v32
	v_lshlrev_b32_e32 v28, 4, v28
	v_add_f32_e32 v22, v22, v66
	v_add_f32_e32 v23, v23, v67
	v_add_f32_e32 v18, v18, v66
	v_add_f32_e32 v19, v19, v67
	v_add_f32_e32 v14, v14, v66
	v_add_f32_e32 v15, v15, v67
	v_add_f32_e32 v10, v10, v66
	v_add_f32_e32 v11, v11, v67
	v_add_f32_e32 v6, v6, v66
	v_add_f32_e32 v7, v7, v67
	v_max_f32_e32 v2, 0, v2
	v_add_f32_e32 v3, v3, v67
	v_add3_u32 v32, v103, v32, v102
	v_add3_u32 v28, v103, v28, v102
	v_max_f32_e32 v22, 0, v22
	v_max_f32_e32 v23, 0, v23
	v_add_f32_e32 v24, v24, v68
	v_add_f32_e32 v25, v25, v69
	v_max_f32_e32 v18, 0, v18
	v_max_f32_e32 v19, 0, v19
	v_add_f32_e32 v20, v20, v68
	v_add_f32_e32 v21, v21, v69
	v_max_f32_e32 v14, 0, v14
	v_max_f32_e32 v15, 0, v15
	v_add_f32_e32 v16, v16, v68
	v_add_f32_e32 v17, v17, v69
	v_max_f32_e32 v10, 0, v10
	v_max_f32_e32 v11, 0, v11
	v_add_f32_e32 v12, v12, v68
	v_add_f32_e32 v13, v13, v69
	v_max_f32_e32 v6, 0, v6
	v_max_f32_e32 v7, 0, v7
	v_add_f32_e32 v8, v8, v68
	v_add_f32_e32 v9, v9, v69
	v_max_f32_e32 v3, 0, v3
	v_add_f32_e32 v4, v4, v68
	v_add_f32_e32 v5, v5, v69
	v_cvt_pk_bf16_f32 v2, v2, v3
	ds_write_b64 v32, v[30:31]
	ds_write_b64 v28, v[26:27] offset:8192
	v_max_f32_e32 v24, 0, v24
	v_max_f32_e32 v25, 0, v25
	v_cvt_pk_bf16_f32 v22, v22, v23
	v_cvt_pk_bf16_f32 v23, v24, v25
	ds_write_b64 v32, v[22:23] offset:16384
	v_max_f32_e32 v20, 0, v20
	v_max_f32_e32 v21, 0, v21
	v_cvt_pk_bf16_f32 v18, v18, v19
	v_cvt_pk_bf16_f32 v19, v20, v21
	ds_write_b64 v28, v[18:19] offset:24576
	v_max_f32_e32 v16, 0, v16
	v_max_f32_e32 v17, 0, v17
	v_cvt_pk_bf16_f32 v14, v14, v15
	v_cvt_pk_bf16_f32 v15, v16, v17
	ds_write_b64 v32, v[14:15] offset:32768
	v_max_f32_e32 v12, 0, v12
	v_max_f32_e32 v13, 0, v13
	v_cvt_pk_bf16_f32 v10, v10, v11
	v_cvt_pk_bf16_f32 v11, v12, v13
	ds_write_b64 v28, v[10:11] offset:40960
	v_max_f32_e32 v8, 0, v8
	v_max_f32_e32 v9, 0, v9
	v_cvt_pk_bf16_f32 v6, v6, v7
	v_cvt_pk_bf16_f32 v7, v8, v9
	ds_write_b64 v32, v[6:7] offset:49152
	v_max_f32_e32 v4, 0, v4
	v_max_f32_e32 v5, 0, v5
	v_cvt_pk_bf16_f32 v3, v4, v5
	ds_write_b64 v28, v[2:3] offset:57344
	v_and_b32_e32 v2, 0x1f0, v1
	v_lshrrev_b32_e32 v1, 5, v0
	v_xor_b32_e32 v4, v1, v0
	v_mov_b32_e32 v3, 0
	v_lshlrev_b32_e32 v4, 4, v4
	v_lshl_add_u64 v[12:13], s[4:5], 0, v[2:3]
	v_lshlrev_b32_e32 v2, 9, v1
	v_and_b32_e32 v16, 0x1f0, v4
	v_add3_u32 v2, 0, v2, v16
	s_waitcnt lgkmcnt(0)
	s_barrier
	ds_read_b128 v[4:7], v2
	v_lshlrev_b32_e32 v2, 11, v1
	v_lshl_add_u64 v[14:15], v[12:13], 0, v[2:3]
	v_or_b32_e32 v2, 0x200, v0
	v_lshrrev_b32_e32 v2, 5, v2
	v_xor_b32_e32 v9, v2, v0
	v_lshlrev_b32_e32 v9, 4, v9
	v_lshlrev_b32_e32 v8, 9, v2
	v_and_b32_e32 v9, 0x1f0, v9
	v_add3_u32 v8, 0, v8, v9
	ds_read_b128 v[8:11], v8
	v_lshlrev_b32_e32 v2, 11, v2
	s_waitcnt lgkmcnt(1)
	global_store_dwordx4 v[14:15], v[4:7], off sc1
	s_nop 1
	v_lshl_add_u64 v[4:5], v[12:13], 0, v[2:3]
	s_waitcnt lgkmcnt(0)
	global_store_dwordx4 v[4:5], v[8:11], off sc1
	v_or_b32_e32 v2, 32, v1
	v_lshlrev_b32_e32 v4, 9, v2
	v_or_b32_e32 v8, 0x600, v0
	v_lshrrev_b32_e32 v17, 5, v8
	v_xor_b32_e32 v9, v17, v0
	v_lshlrev_b32_e32 v9, 4, v9
	v_add3_u32 v4, 0, v4, v16
	v_lshlrev_b32_e32 v8, 9, v17
	v_and_b32_e32 v9, 0x1f0, v9
	ds_read_b128 v[4:7], v4
	v_add3_u32 v8, 0, v8, v9
	ds_read_b128 v[8:11], v8
	v_lshlrev_b32_e32 v2, 11, v2
	v_lshl_add_u64 v[14:15], v[12:13], 0, v[2:3]
	v_lshlrev_b32_e32 v2, 11, v17
	s_waitcnt lgkmcnt(1)
	global_store_dwordx4 v[14:15], v[4:7], off sc1
	s_nop 1
	v_lshl_add_u64 v[4:5], v[12:13], 0, v[2:3]
	s_waitcnt lgkmcnt(0)
	global_store_dwordx4 v[4:5], v[8:11], off sc1
	v_or_b32_e32 v2, 64, v1
	v_lshlrev_b32_e32 v4, 9, v2
	v_or_b32_e32 v8, 0xa00, v0
	v_lshrrev_b32_e32 v17, 5, v8
	v_xor_b32_e32 v9, v17, v0
	v_lshlrev_b32_e32 v9, 4, v9
	v_add3_u32 v4, 0, v4, v16
	v_lshlrev_b32_e32 v8, 9, v17
	v_and_b32_e32 v9, 0x1f0, v9
	ds_read_b128 v[4:7], v4
	v_add3_u32 v8, 0, v8, v9
	ds_read_b128 v[8:11], v8
	v_lshlrev_b32_e32 v2, 11, v2
	v_lshl_add_u64 v[14:15], v[12:13], 0, v[2:3]
	v_lshlrev_b32_e32 v2, 11, v17
	s_waitcnt lgkmcnt(1)
	global_store_dwordx4 v[14:15], v[4:7], off sc1
	s_nop 1
	v_lshl_add_u64 v[4:5], v[12:13], 0, v[2:3]
	s_waitcnt lgkmcnt(0)
	global_store_dwordx4 v[4:5], v[8:11], off sc1
	v_or_b32_e32 v2, 0x60, v1
	v_lshlrev_b32_e32 v4, 9, v2
	v_or_b32_e32 v8, 0xe00, v0
	v_lshrrev_b32_e32 v17, 5, v8
	v_xor_b32_e32 v9, v17, v0
	v_lshlrev_b32_e32 v9, 4, v9
	v_add3_u32 v4, 0, v4, v16
	v_lshlrev_b32_e32 v8, 9, v17
	v_and_b32_e32 v9, 0x1f0, v9
	ds_read_b128 v[4:7], v4
	v_add3_u32 v8, 0, v8, v9
	ds_read_b128 v[8:11], v8
	v_lshlrev_b32_e32 v2, 11, v2
	v_lshl_add_u64 v[14:15], v[12:13], 0, v[2:3]
	v_lshlrev_b32_e32 v2, 11, v17
	s_waitcnt lgkmcnt(1)
	global_store_dwordx4 v[14:15], v[4:7], off sc1
	s_nop 1
	v_lshl_add_u64 v[4:5], v[12:13], 0, v[2:3]
	s_waitcnt lgkmcnt(0)
	global_store_dwordx4 v[4:5], v[8:11], off sc1
	v_or_b32_e32 v2, 0x80, v1
	v_lshlrev_b32_e32 v4, 9, v2
	v_or_b32_e32 v8, 0x1200, v0
	v_lshrrev_b32_e32 v17, 5, v8
	v_xor_b32_e32 v9, v17, v0
	v_lshlrev_b32_e32 v9, 4, v9
	v_add3_u32 v4, 0, v4, v16
	v_lshlrev_b32_e32 v8, 9, v17
	v_and_b32_e32 v9, 0x1f0, v9
	ds_read_b128 v[4:7], v4
	v_add3_u32 v8, 0, v8, v9
	ds_read_b128 v[8:11], v8
	v_lshlrev_b32_e32 v2, 11, v2
	v_lshl_add_u64 v[14:15], v[12:13], 0, v[2:3]
	v_lshlrev_b32_e32 v2, 11, v17
	s_waitcnt lgkmcnt(1)
	global_store_dwordx4 v[14:15], v[4:7], off sc1
	s_nop 1
	v_lshl_add_u64 v[4:5], v[12:13], 0, v[2:3]
	s_waitcnt lgkmcnt(0)
	global_store_dwordx4 v[4:5], v[8:11], off sc1
	v_or_b32_e32 v2, 0xa0, v1
	v_lshlrev_b32_e32 v4, 9, v2
	v_or_b32_e32 v8, 0x1600, v0
	v_lshrrev_b32_e32 v17, 5, v8
	v_xor_b32_e32 v9, v17, v0
	v_lshlrev_b32_e32 v9, 4, v9
	v_add3_u32 v4, 0, v4, v16
	v_lshlrev_b32_e32 v8, 9, v17
	v_and_b32_e32 v9, 0x1f0, v9
	ds_read_b128 v[4:7], v4
	v_add3_u32 v8, 0, v8, v9
	ds_read_b128 v[8:11], v8
	v_lshlrev_b32_e32 v2, 11, v2
	v_lshl_add_u64 v[14:15], v[12:13], 0, v[2:3]
	v_lshlrev_b32_e32 v2, 11, v17
	s_waitcnt lgkmcnt(1)
	global_store_dwordx4 v[14:15], v[4:7], off sc1
	s_nop 1
	v_lshl_add_u64 v[4:5], v[12:13], 0, v[2:3]
	s_waitcnt lgkmcnt(0)
	global_store_dwordx4 v[4:5], v[8:11], off sc1
	v_or_b32_e32 v2, 0xc0, v1
	v_lshlrev_b32_e32 v4, 9, v2
	v_or_b32_e32 v8, 0x1a00, v0
	v_lshrrev_b32_e32 v17, 5, v8
	v_xor_b32_e32 v9, v17, v0
	v_add3_u32 v4, 0, v4, v16
	v_lshlrev_b32_e32 v9, 4, v9
	ds_read_b128 v[4:7], v4
	v_lshlrev_b32_e32 v8, 9, v17
	v_and_b32_e32 v9, 0x1f0, v9
	v_add3_u32 v8, 0, v8, v9
	ds_read_b128 v[8:11], v8
	v_lshlrev_b32_e32 v2, 11, v2
	v_lshl_add_u64 v[14:15], v[12:13], 0, v[2:3]
	v_lshlrev_b32_e32 v2, 11, v17
	v_or_b32_e32 v1, 0xe0, v1
	s_waitcnt lgkmcnt(1)
	global_store_dwordx4 v[14:15], v[4:7], off sc1
	s_nop 1
	v_lshl_add_u64 v[4:5], v[12:13], 0, v[2:3]
	v_lshlrev_b32_e32 v2, 9, v1
	v_add3_u32 v2, 0, v2, v16
	s_waitcnt lgkmcnt(0)
	global_store_dwordx4 v[4:5], v[8:11], off sc1
	ds_read_b128 v[4:7], v2
	v_lshlrev_b32_e32 v2, 11, v1
	v_or_b32_e32 v1, 0x1e00, v0
	v_lshrrev_b32_e32 v1, 5, v1
	v_xor_b32_e32 v9, v1, v0
	v_lshlrev_b32_e32 v9, 4, v9
	v_lshlrev_b32_e32 v8, 9, v1
	v_and_b32_e32 v9, 0x1f0, v9
	v_add3_u32 v8, 0, v8, v9
	ds_read_b128 v[8:11], v8
	v_lshl_add_u64 v[14:15], v[12:13], 0, v[2:3]
	v_lshlrev_b32_e32 v2, 11, v1
	s_waitcnt lgkmcnt(1)
	global_store_dwordx4 v[14:15], v[4:7], off sc1
	s_nop 1
	v_lshl_add_u64 v[4:5], v[12:13], 0, v[2:3]
	s_waitcnt lgkmcnt(0)
	global_store_dwordx4 v[4:5], v[8:11], off sc1
	s_waitcnt lgkmcnt(0)
	s_barrier
	s_lshl_b32 s3, s2, 3
	s_and_b32 s3, s3, 56
	s_ashr_i32 s17, s2, 5
	s_add_i32 s20, s3, s17
	s_ashr_i32 s21, s20, 31
	s_bfe_u32 s16, s2, 0x20003
	s_lshl_b64 s[4:5], s[20:21], 17
	s_lshl_b64 s[6:7], s[20:21], 19
	s_add_u32 s6, s12, s6
	s_addc_u32 s7, s13, s7
	s_lshl_b32 s3, s16, 19
	s_add_u32 s3, s14, s3
	v_ashrrev_i32_e32 v2, 6, v0
	v_lshlrev_b32_e32 v1, 4, v0
	s_addc_u32 s13, s15, 0
	v_lshlrev_b32_e32 v4, 9, v2
	v_and_b32_e32 v5, 0x1f0, v1
	s_add_u32 s12, s3, 0x400000
	v_and_or_b32 v32, v4, s0, v5
	v_lshlrev_b32_e32 v4, 5, v2
	v_and_b32_e32 v5, 48, v1
	s_addc_u32 s13, s13, 0
	v_bitop3_b32 v4, v4, v5, 32 bitop3:0x6c
	s_and_b32 s15, s2, 8
	s_add_i32 s3, s20, 3
	v_bfe_u32 v31, v0, 5, 1
	v_lshrrev_b32_e32 v34, 1, v4
	v_add_u32_e32 v4, s15, v2
	s_mov_b32 s20, 0x3ffffe
	v_and_or_b32 v30, v4, s20, v31
	v_bfe_i32 v5, v30, 0, 22
	v_bfe_u32 v4, v30, 21, 1
	v_add_u32_e32 v6, v5, v4
	v_lshlrev_b32_e32 v4, 3, v6
	v_and_b32_e32 v6, 0x7fffffe, v6
	s_lshl_b32 s0, s17, 4
	v_sub_u32_e32 v5, v5, v6
	s_and_b32 s17, s0, 16
	v_lshl_or_b32 v6, v5, 5, v34
	v_add_u32_e32 v5, s17, v2
	v_and_or_b32 v35, v5, s20, v31
	v_bfe_i32 v7, v35, 0, 22
	v_bfe_u32 v8, v35, 21, 1
	v_add_u32_e32 v8, v7, v8
	v_lshlrev_b32_e32 v9, 3, v8
	v_and_b32_e32 v8, 0x7fffffe, v8
	v_add_u32_e32 v5, 8, v5
	v_sub_u32_e32 v7, v7, v8
	v_and_or_b32 v36, v5, s20, v31
	v_lshl_or_b32 v98, v7, 5, v34
	v_bfe_i32 v5, v36, 0, 22
	v_bfe_u32 v7, v36, 21, 1
	v_add_u32_e32 v7, v5, v7
	v_lshrrev_b32_e32 v33, 6, v32
	v_lshlrev_b32_e32 v8, 3, v7
	v_and_b32_e32 v7, 0x7fffffe, v7
	s_and_b32 s3, s3, 15
	v_and_or_b32 v4, v4, -16, v33
	v_sub_u32_e32 v5, v5, v7
	v_and_or_b32 v14, v9, -16, v33
	v_lshl_or_b32 v100, v5, 5, v34
	v_ashrrev_i32_e32 v5, 31, v4
	s_lshl_b32 s14, s3, 6
	s_lshl_b32 s0, s3, 8
	s_lshl_b32 s2, s3, 7
	v_and_or_b32 v16, v8, -16, v33
	v_lshlrev_b64 v[4:5], 12, v[4:5]
	s_add_u32 s2, s12, s2
	v_ashrrev_i32_e32 v15, 31, v14
	v_lshl_add_u64 v[4:5], s[6:7], 0, v[4:5]
	v_ashrrev_i32_e32 v7, 31, v6
	s_addc_u32 s3, s13, 0
	v_lshlrev_b64 v[102:103], 11, v[14:15]
	v_ashrrev_i32_e32 v99, 31, v98
	v_ashrrev_i32_e32 v17, 31, v16
	v_lshl_add_u64 v[8:9], v[4:5], 0, s[0:1]
	v_lshlrev_b64 v[38:39], 2, v[6:7]
	v_lshl_add_u64 v[14:15], s[2:3], 0, v[102:103]
	v_lshlrev_b64 v[22:23], 1, v[98:99]
	v_lshlrev_b64 v[104:105], 11, v[16:17]
	v_ashrrev_i32_e32 v101, 31, v100
	v_lshl_add_u64 v[18:19], v[8:9], 0, v[38:39]
	v_lshl_add_u64 v[24:25], v[14:15], 0, v[22:23]
	v_lshl_add_u64 v[14:15], s[2:3], 0, v[104:105]
	v_lshlrev_b64 v[26:27], 1, v[100:101]
	global_load_dwordx4 v[6:9], v[18:19], off offset:16
	global_load_dwordx4 v[10:13], v[18:19], off
	v_lshl_add_u64 v[28:29], v[14:15], 0, v[26:27]
	global_load_dwordx4 v[14:17], v[24:25], off
	global_load_dwordx4 v[18:21], v[28:29], off
	v_lshlrev_b32_e32 v24, 10, v30
	v_or_b32_e32 v125, v24, v32
	v_xad_u32 v24, s15, 8, v2
	v_and_or_b32 v24, v24, s20, v31
	v_lshlrev_b32_e32 v25, 10, v24
	v_or_b32_e32 v122, v25, v32
	v_bfe_i32 v25, v24, 0, 22
	v_bfe_u32 v24, v24, 21, 1
	v_add_u32_e32 v28, v25, v24
	v_lshlrev_b32_e32 v24, 3, v28
	v_and_b32_e32 v28, 0x7fffffe, v28
	v_sub_u32_e32 v25, v25, v28
	v_lshl_or_b32 v28, v25, 5, v34
	v_lshlrev_b32_e32 v25, 10, v35
	v_or_b32_e32 v126, v25, v32
	v_lshlrev_b32_e32 v25, 10, v36
	v_or_b32_e32 v127, v25, v32
	v_xad_u32 v25, s17, 16, v2
	v_and_or_b32 v25, v25, s20, v31
	v_lshlrev_b32_e32 v29, 10, v25
	v_or_b32_e32 v123, v29, v32
	v_bfe_i32 v29, v25, 0, 22
	v_bfe_u32 v25, v25, 21, 1
	v_add_u32_e32 v25, v29, v25
	v_and_b32_e32 v121, 3, v2
	v_lshlrev_b32_e32 v30, 3, v25
	v_and_b32_e32 v25, 0x7fffffe, v25
	v_xad_u32 v2, s17, 24, v2
	v_sub_u32_e32 v25, v29, v25
	v_and_or_b32 v2, v2, s20, v31
	v_lshl_or_b32 v106, v25, 5, v34
	v_lshlrev_b32_e32 v25, 10, v2
	v_or_b32_e32 v124, v25, v32
	v_bfe_i32 v25, v2, 0, 22
	v_bfe_u32 v2, v2, 21, 1
	v_add_u32_e32 v2, v25, v2
	v_lshlrev_b32_e32 v29, 3, v2
	v_and_b32_e32 v2, 0x7fffffe, v2
	v_and_b32_e32 v118, 15, v0
	v_sub_u32_e32 v2, v25, v2
	v_lshlrev_b32_e32 v25, 2, v0
	v_ashrrev_i32_e32 v120, 8, v0
	v_and_or_b32 v32, v29, -16, v33
	v_lshl_or_b32 v108, v2, 5, v34
	v_and_b32_e32 v2, 48, v0
	v_and_b32_e32 v25, 32, v25
	v_lshlrev_b32_e32 v29, 6, v118
	v_and_b32_e32 v119, 63, v0
	v_and_or_b32 v24, v24, -16, v33
	v_and_or_b32 v30, v30, -16, v33
	v_lshlrev_b32_e32 v68, 13, v120
	v_bitop3_b32 v2, v29, v25, v2 bitop3:0x36
	v_ashrrev_i32_e32 v25, 31, v24
	v_lshlrev_b64 v[24:25], 12, v[24:25]
	v_lshl_add_u64 v[56:57], s[6:7], 0, v[24:25]
	v_ashrrev_i32_e32 v29, 31, v28
	v_lshl_add_u64 v[24:25], v[56:57], 0, s[0:1]
	v_lshlrev_b64 v[58:59], 2, v[28:29]
	v_ashrrev_i32_e32 v31, 31, v30
	v_lshl_add_u64 v[24:25], v[24:25], 0, v[58:59]
	v_lshlrev_b64 v[110:111], 11, v[30:31]
	v_ashrrev_i32_e32 v107, 31, v106
	v_ashrrev_i32_e32 v33, 31, v32
	global_load_dwordx4 v[40:43], v[24:25], off offset:16
	global_load_dwordx4 v[44:47], v[24:25], off
	v_lshl_add_u64 v[24:25], s[2:3], 0, v[110:111]
	v_lshlrev_b64 v[60:61], 1, v[106:107]
	v_lshlrev_b64 v[112:113], 11, v[32:33]
	v_ashrrev_i32_e32 v109, 31, v108
	v_lshl_add_u64 v[24:25], v[24:25], 0, v[60:61]
	v_lshl_add_u64 v[28:29], s[2:3], 0, v[112:113]
	v_lshlrev_b64 v[62:63], 1, v[108:109]
	v_lshl_add_u64 v[28:29], v[28:29], 0, v[62:63]
	global_load_dwordx4 v[48:51], v[24:25], off
	global_load_dwordx4 v[52:55], v[28:29], off
	s_add_i32 s0, s14, 64
	s_and_b32 s2, s0, 0x3c0
	s_lshl_b32 s0, s2, 2
	s_lshl_b32 s2, s2, 1
	v_lshl_add_u64 v[24:25], v[4:5], 0, s[0:1]
	s_add_u32 s2, s12, s2
	v_lshl_add_u64 v[24:25], v[24:25], 0, v[38:39]
	s_addc_u32 s3, s13, 0
	global_load_dwordx4 v[30:33], v[24:25], off offset:16
	global_load_dwordx4 v[34:37], v[24:25], off
	v_lshl_add_u64 v[24:25], s[2:3], 0, v[102:103]
	v_lshl_add_u64 v[64:65], v[24:25], 0, v[22:23]
	v_lshl_add_u64 v[22:23], s[2:3], 0, v[104:105]
	v_lshl_add_u64 v[66:67], v[22:23], 0, v[26:27]
	global_load_dwordx4 v[26:29], v[64:65], off
	global_load_dwordx4 v[22:25], v[66:67], off
	v_add_u32_e32 v64, 0, v125
	s_waitcnt vmcnt(10)
	v_cvt_pk_bf16_f32 v10, v10, v11
	v_cvt_pk_bf16_f32 v11, v12, v13
	v_cvt_pk_bf16_f32 v12, v6, v7
	v_add_u32_e32 v6, 0, v126
	v_cvt_pk_bf16_f32 v13, v8, v9
	ds_write_b128 v64, v[10:13]
	s_waitcnt vmcnt(9)
	ds_write_b128 v6, v[14:17] offset:32768
	v_add_u32_e32 v6, 0, v127
	s_waitcnt vmcnt(8)
	ds_write_b128 v6, v[18:21] offset:32768
	v_add_u32_e32 v10, 0, v122
	s_waitcnt vmcnt(6)
	v_cvt_pk_bf16_f32 v6, v44, v45
	v_cvt_pk_bf16_f32 v7, v46, v47
	v_cvt_pk_bf16_f32 v8, v40, v41
	v_cvt_pk_bf16_f32 v9, v42, v43
	ds_write_b128 v10, v[6:9]
	v_add_u32_e32 v6, 0, v123
	s_waitcnt vmcnt(5)
	ds_write_b128 v6, v[48:51] offset:32768
	v_add_u32_e32 v6, 0, v124
	s_waitcnt vmcnt(4)
	ds_write_b128 v6, v[52:55] offset:32768
	v_lshl_add_u64 v[6:7], v[56:57], 0, s[0:1]
	v_lshl_add_u64 v[14:15], v[6:7], 0, v[58:59]
	global_load_dwordx4 v[6:9], v[14:15], off offset:16
	global_load_dwordx4 v[10:13], v[14:15], off
	v_lshl_add_u64 v[14:15], s[2:3], 0, v[110:111]
	v_lshl_add_u64 v[40:41], v[14:15], 0, v[60:61]
	v_lshl_add_u64 v[14:15], s[2:3], 0, v[112:113]
	v_lshl_add_u64 v[42:43], v[14:15], 0, v[62:63]
	global_load_dwordx4 v[18:21], v[40:41], off
	global_load_dwordx4 v[14:17], v[42:43], off
	v_lshlrev_b32_e32 v40, 13, v121
	s_cmp_lg_u32 0, -1
	s_waitcnt lgkmcnt(0)
	s_cselect_b32 s0, 0, 0
	v_add3_u32 v128, v68, s0, v2
	s_add_i32 s0, s0, 0x8000
	v_add3_u32 v129, v40, s0, v2
	v_lshl_add_u64 v[114:115], v[4:5], 0, v[38:39]
	v_lshl_add_u64 v[116:117], v[56:57], 0, v[58:59]
	s_add_i32 s2, s14, 0x80
	s_mov_b32 s3, 0
	v_mov_b32_e32 v2, v3
	v_mov_b32_e32 v4, v3
	v_mov_b32_e32 v5, v3
	v_mov_b32_e32 v38, v3
	v_mov_b32_e32 v39, v3
	v_mov_b32_e32 v40, v3
	v_mov_b32_e32 v41, v3
	v_mov_b32_e32 v42, v3
	v_mov_b32_e32 v43, v3
	v_mov_b32_e32 v44, v3
	v_mov_b32_e32 v45, v3
	v_mov_b32_e32 v46, v3
	v_mov_b32_e32 v47, v3
	v_mov_b32_e32 v48, v3
	v_mov_b32_e32 v49, v3
	v_mov_b32_e32 v50, v3
	v_mov_b32_e32 v51, v3
	v_mov_b32_e32 v52, v3
	v_mov_b32_e32 v53, v3
	v_mov_b32_e32 v54, v3
	v_mov_b32_e32 v55, v3
	v_mov_b32_e32 v56, v3
	v_mov_b32_e32 v57, v3
	v_mov_b32_e32 v58, v3
	v_mov_b32_e32 v59, v3
	v_mov_b32_e32 v60, v3
	v_mov_b32_e32 v61, v3
	v_mov_b32_e32 v62, v3
	v_mov_b32_e32 v63, v3
	v_mov_b32_e32 v64, v3
	v_mov_b32_e32 v65, v3
	v_mov_b32_e32 v66, v3
	v_mov_b32_e32 v67, v3
	v_mov_b32_e32 v68, v3
	v_mov_b32_e32 v69, v3
	v_mov_b32_e32 v70, v3
	v_mov_b32_e32 v71, v3
	v_mov_b32_e32 v72, v3
	v_mov_b32_e32 v73, v3
	v_mov_b32_e32 v74, v3
	v_mov_b32_e32 v75, v3
	v_mov_b32_e32 v76, v3
	v_mov_b32_e32 v77, v3
	v_mov_b32_e32 v78, v3
	v_mov_b32_e32 v79, v3
	v_mov_b32_e32 v80, v3
	v_mov_b32_e32 v81, v3
	v_mov_b32_e32 v82, v3
	v_mov_b32_e32 v83, v3
	v_mov_b32_e32 v84, v3
	v_mov_b32_e32 v85, v3
	v_mov_b32_e32 v86, v3
	v_mov_b32_e32 v87, v3
	v_mov_b32_e32 v88, v3
	v_mov_b32_e32 v89, v3
	v_mov_b32_e32 v90, v3
	v_mov_b32_e32 v91, v3
	v_mov_b32_e32 v92, v3
	v_mov_b32_e32 v93, v3
	v_mov_b32_e32 v94, v3
	v_mov_b32_e32 v95, v3
	v_mov_b32_e32 v96, v3
	v_mov_b32_e32 v97, v3
	s_barrier
.LBB1_3:
	s_and_b32 s0, s3, 0x10000
	v_add_u32_e32 v158, s0, v128
	v_add_u32_e32 v159, s0, v129
	ds_read_b128 v[130:133], v159 offset:0
	ds_read_b128 v[134:137], v159 offset:0x800
	ds_read_b128 v[138:141], v159 offset:0x1000
	ds_read_b128 v[142:145], v159 offset:0x1800
	ds_read_b128 v[146:149], v158 offset:0
	ds_read_b128 v[150:153], v158 offset:0x800
	ds_read_b128 v[154:157], v158 offset:0x1000
	s_waitcnt lgkmcnt(2)
	v_mfma_f32_16x16x32_bf16 v[94:97], v[130:133], v[146:149], v[94:97]
	v_mfma_f32_16x16x32_bf16 v[90:93], v[134:137], v[146:149], v[90:93]
	v_mfma_f32_16x16x32_bf16 v[86:89], v[138:141], v[146:149], v[86:89]
	v_mfma_f32_16x16x32_bf16 v[82:85], v[142:145], v[146:149], v[82:85]
	ds_read_b128 v[146:149], v158 offset:0x1800
	s_waitcnt lgkmcnt(2)
	v_mfma_f32_16x16x32_bf16 v[78:81], v[130:133], v[150:153], v[78:81]
	v_mfma_f32_16x16x32_bf16 v[74:77], v[134:137], v[150:153], v[74:77]
	v_mfma_f32_16x16x32_bf16 v[70:73], v[138:141], v[150:153], v[70:73]
	v_mfma_f32_16x16x32_bf16 v[66:69], v[142:145], v[150:153], v[66:69]
	s_waitcnt lgkmcnt(1)
	v_mfma_f32_16x16x32_bf16 v[62:65], v[130:133], v[154:157], v[62:65]
	v_mfma_f32_16x16x32_bf16 v[58:61], v[134:137], v[154:157], v[58:61]
	v_mfma_f32_16x16x32_bf16 v[54:57], v[138:141], v[154:157], v[54:57]
	v_mfma_f32_16x16x32_bf16 v[50:53], v[142:145], v[154:157], v[50:53]
	s_waitcnt lgkmcnt(0)
	v_mfma_f32_16x16x32_bf16 v[46:49], v[130:133], v[146:149], v[46:49]
	v_mfma_f32_16x16x32_bf16 v[42:45], v[134:137], v[146:149], v[42:45]
	v_mfma_f32_16x16x32_bf16 v[38:41], v[138:141], v[146:149], v[38:41]
	v_mfma_f32_16x16x32_bf16 v[2:5], v[142:145], v[146:149], v[2:5]
	s_xor_b32 s0, s0, 0x10000
	s_and_b32 s6, s2, 0x3c0
	s_add_i32 s14, s0, 0
	s_lshl_b32 s0, s6, 2
	s_lshl_b32 s6, s6, 1
	s_add_u32 s6, s12, s6
	s_waitcnt vmcnt(6)
	v_cvt_pk_bf16_f32 v34, v34, v35
	v_cvt_pk_bf16_f32 v35, v36, v37
	v_cvt_pk_bf16_f32 v36, v30, v31
	v_cvt_pk_bf16_f32 v37, v32, v33
	v_add_u32_e32 v30, s14, v125
	s_addc_u32 s7, s13, 0
	v_add_u32_e32 v31, s14, v126
	v_add_u32_e32 v32, s14, v127
	ds_write_b128 v30, v[34:37]
	s_waitcnt vmcnt(5)
	ds_write_b128 v31, v[26:29] offset:32768
	s_waitcnt vmcnt(4)
	ds_write_b128 v32, v[22:25] offset:32768
	v_lshl_add_u64 v[22:23], s[6:7], 0, v[102:103]
	v_lshl_add_u64 v[24:25], s[6:7], 0, v[104:105]
	v_lshl_add_u64 v[130:131], v[114:115], 0, s[0:1]
	v_lshl_add_u64 v[22:23], v[98:99], 1, v[22:23]
	v_lshl_add_u64 v[24:25], v[100:101], 1, v[24:25]
	global_load_dwordx4 v[30:33], v[130:131], off offset:16
	global_load_dwordx4 v[34:37], v[130:131], off
	global_load_dwordx4 v[26:29], v[22:23], off
	s_nop 0
	global_load_dwordx4 v[22:25], v[24:25], off
	ds_read_b128 v[130:133], v159 offset:0x400
	ds_read_b128 v[134:137], v159 offset:0xc00
	ds_read_b128 v[138:141], v159 offset:0x1400
	ds_read_b128 v[142:145], v159 offset:0x1c00
	ds_read_b128 v[146:149], v158 offset:0x400
	ds_read_b128 v[150:153], v158 offset:0xc00
	ds_read_b128 v[154:157], v158 offset:0x1400
	s_waitcnt lgkmcnt(2)
	v_mfma_f32_16x16x32_bf16 v[94:97], v[130:133], v[146:149], v[94:97]
	v_mfma_f32_16x16x32_bf16 v[90:93], v[134:137], v[146:149], v[90:93]
	v_mfma_f32_16x16x32_bf16 v[86:89], v[138:141], v[146:149], v[86:89]
	v_mfma_f32_16x16x32_bf16 v[82:85], v[142:145], v[146:149], v[82:85]
	ds_read_b128 v[146:149], v158 offset:0x1c00
	s_waitcnt lgkmcnt(2)
	v_mfma_f32_16x16x32_bf16 v[78:81], v[130:133], v[150:153], v[78:81]
	v_mfma_f32_16x16x32_bf16 v[74:77], v[134:137], v[150:153], v[74:77]
	v_mfma_f32_16x16x32_bf16 v[70:73], v[138:141], v[150:153], v[70:73]
	v_mfma_f32_16x16x32_bf16 v[66:69], v[142:145], v[150:153], v[66:69]
	s_waitcnt lgkmcnt(1)
	v_mfma_f32_16x16x32_bf16 v[62:65], v[130:133], v[154:157], v[62:65]
	v_mfma_f32_16x16x32_bf16 v[58:61], v[134:137], v[154:157], v[58:61]
	v_mfma_f32_16x16x32_bf16 v[54:57], v[138:141], v[154:157], v[54:57]
	v_mfma_f32_16x16x32_bf16 v[50:53], v[142:145], v[154:157], v[50:53]
	s_waitcnt lgkmcnt(0)
	v_mfma_f32_16x16x32_bf16 v[46:49], v[130:133], v[146:149], v[46:49]
	v_mfma_f32_16x16x32_bf16 v[42:45], v[134:137], v[146:149], v[42:45]
	v_mfma_f32_16x16x32_bf16 v[38:41], v[138:141], v[146:149], v[38:41]
	v_mfma_f32_16x16x32_bf16 v[2:5], v[142:145], v[146:149], v[2:5]
	v_add_u32_e32 v130, s14, v122
	s_waitcnt vmcnt(6)
	v_cvt_pk_bf16_f32 v10, v10, v11
	v_cvt_pk_bf16_f32 v11, v12, v13
	v_cvt_pk_bf16_f32 v12, v6, v7
	v_add_u32_e32 v6, s14, v123
	v_cvt_pk_bf16_f32 v13, v8, v9
	ds_write_b128 v130, v[10:13]
	s_waitcnt vmcnt(5)
	ds_write_b128 v6, v[18:21] offset:32768
	v_add_u32_e32 v6, s14, v124
	s_waitcnt vmcnt(4)
	ds_write_b128 v6, v[14:17] offset:32768
	v_lshl_add_u64 v[14:15], s[6:7], 0, v[110:111]
	v_lshl_add_u64 v[16:17], s[6:7], 0, v[112:113]
	v_lshl_add_u64 v[10:11], v[116:117], 0, s[0:1]
	v_lshl_add_u64 v[14:15], v[106:107], 1, v[14:15]
	v_lshl_add_u64 v[16:17], v[108:109], 1, v[16:17]
	global_load_dwordx4 v[6:9], v[10:11], off offset:16
	s_nop 0
	global_load_dwordx4 v[10:13], v[10:11], off
	s_nop 0
	global_load_dwordx4 v[18:21], v[14:15], off
	s_nop 0
	global_load_dwordx4 v[14:17], v[16:17], off
	s_waitcnt lgkmcnt(0)
	s_add_i32 s2, s2, 64
	s_add_i32 s3, s3, 0x10000
	s_cmp_lg_u32 s3, 0xe0000
	s_barrier
	s_cbranch_scc1 .LBB1_3
	ds_read_b128 v[98:101], v129 offset:0
	ds_read_b128 v[102:105], v129 offset:0x800
	ds_read_b128 v[106:109], v129 offset:0x1000
	ds_read_b128 v[110:113], v129 offset:0x1800
	ds_read_b128 v[114:117], v128 offset:0
	ds_read_b128 v[130:133], v128 offset:0x800
	ds_read_b128 v[134:137], v128 offset:0x1000
	s_waitcnt lgkmcnt(2)
	v_mfma_f32_16x16x32_bf16 v[94:97], v[98:101], v[114:117], v[94:97]
	v_mfma_f32_16x16x32_bf16 v[90:93], v[102:105], v[114:117], v[90:93]
	v_mfma_f32_16x16x32_bf16 v[86:89], v[106:109], v[114:117], v[86:89]
	v_mfma_f32_16x16x32_bf16 v[82:85], v[110:113], v[114:117], v[82:85]
	ds_read_b128 v[114:117], v128 offset:0x1800
	s_waitcnt lgkmcnt(2)
	v_mfma_f32_16x16x32_bf16 v[78:81], v[98:101], v[130:133], v[78:81]
	v_mfma_f32_16x16x32_bf16 v[74:77], v[102:105], v[130:133], v[74:77]
	v_mfma_f32_16x16x32_bf16 v[70:73], v[106:109], v[130:133], v[70:73]
	v_mfma_f32_16x16x32_bf16 v[66:69], v[110:113], v[130:133], v[66:69]
	s_waitcnt lgkmcnt(1)
	v_mfma_f32_16x16x32_bf16 v[62:65], v[98:101], v[134:137], v[62:65]
	v_mfma_f32_16x16x32_bf16 v[58:61], v[102:105], v[134:137], v[58:61]
	v_mfma_f32_16x16x32_bf16 v[54:57], v[106:109], v[134:137], v[54:57]
	v_mfma_f32_16x16x32_bf16 v[50:53], v[110:113], v[134:137], v[50:53]
	s_waitcnt lgkmcnt(0)
	v_mfma_f32_16x16x32_bf16 v[46:49], v[98:101], v[114:117], v[46:49]
	v_mfma_f32_16x16x32_bf16 v[42:45], v[102:105], v[114:117], v[42:45]
	v_mfma_f32_16x16x32_bf16 v[38:41], v[106:109], v[114:117], v[38:41]
	v_mfma_f32_16x16x32_bf16 v[2:5], v[110:113], v[114:117], v[2:5]
	v_add_u32_e32 v98, s18, v125
	s_waitcnt vmcnt(6)
	v_cvt_pk_bf16_f32 v34, v34, v35
	v_cvt_pk_bf16_f32 v35, v36, v37
	v_cvt_pk_bf16_f32 v36, v30, v31
	v_add_u32_e32 v30, s19, v126
	v_cvt_pk_bf16_f32 v37, v32, v33
	ds_write_b128 v98, v[34:37]
	s_waitcnt vmcnt(5)
	ds_write_b128 v30, v[26:29]
	v_add_u32_e32 v26, s19, v127
	s_waitcnt vmcnt(4)
	ds_write_b128 v26, v[22:25]
	ds_read_b128 v[22:25], v129 offset:0x400
	ds_read_b128 v[26:29], v129 offset:0xc00
	ds_read_b128 v[30:33], v129 offset:0x1400
	ds_read_b128 v[34:37], v129 offset:0x1c00
	ds_read_b128 v[98:101], v128 offset:0x400
	ds_read_b128 v[102:105], v128 offset:0xc00
	ds_read_b128 v[106:109], v128 offset:0x1400
	s_waitcnt lgkmcnt(2)
	v_mfma_f32_16x16x32_bf16 v[94:97], v[22:25], v[98:101], v[94:97]
	v_mfma_f32_16x16x32_bf16 v[90:93], v[26:29], v[98:101], v[90:93]
	v_mfma_f32_16x16x32_bf16 v[86:89], v[30:33], v[98:101], v[86:89]
	v_mfma_f32_16x16x32_bf16 v[82:85], v[34:37], v[98:101], v[82:85]
	ds_read_b128 v[98:101], v128 offset:0x1c00
	s_waitcnt lgkmcnt(2)
	v_mfma_f32_16x16x32_bf16 v[78:81], v[22:25], v[102:105], v[78:81]
	v_mfma_f32_16x16x32_bf16 v[74:77], v[26:29], v[102:105], v[74:77]
	v_mfma_f32_16x16x32_bf16 v[70:73], v[30:33], v[102:105], v[70:73]
	v_mfma_f32_16x16x32_bf16 v[66:69], v[34:37], v[102:105], v[66:69]
	s_waitcnt lgkmcnt(1)
	v_mfma_f32_16x16x32_bf16 v[62:65], v[22:25], v[106:109], v[62:65]
	v_mfma_f32_16x16x32_bf16 v[58:61], v[26:29], v[106:109], v[58:61]
	v_mfma_f32_16x16x32_bf16 v[54:57], v[30:33], v[106:109], v[54:57]
	v_mfma_f32_16x16x32_bf16 v[50:53], v[34:37], v[106:109], v[50:53]
	s_waitcnt lgkmcnt(0)
	v_mfma_f32_16x16x32_bf16 v[22:25], v[22:25], v[98:101], v[46:49]
	v_mfma_f32_16x16x32_bf16 v[26:29], v[26:29], v[98:101], v[42:45]
	v_mfma_f32_16x16x32_bf16 v[30:33], v[30:33], v[98:101], v[38:41]
	v_mfma_f32_16x16x32_bf16 v[2:5], v[34:37], v[98:101], v[2:5]
	v_add_u32_e32 v34, s18, v122
	s_waitcnt vmcnt(2)
	v_cvt_pk_bf16_f32 v10, v10, v11
	v_cvt_pk_bf16_f32 v11, v12, v13
	v_cvt_pk_bf16_f32 v12, v6, v7
	v_add_u32_e32 v6, s19, v123
	s_lshl_b64 s[0:1], s[4:5], 1
	v_cvt_pk_bf16_f32 v13, v8, v9
	ds_write_b128 v34, v[10:13]
	s_waitcnt vmcnt(1)
	ds_write_b128 v6, v[18:21]
	v_add_u32_e32 v6, s19, v124
	s_add_u32 s0, s10, s0
	s_waitcnt vmcnt(0)
	ds_write_b128 v6, v[14:17]
	s_addc_u32 s1, s11, s1
	s_lshl_b32 s2, s16, 9
	s_waitcnt lgkmcnt(0)
	s_barrier
	v_add_u32_e32 v110, 0x10000, v128
	v_add_u32_e32 v102, 0x10000, v129
	ds_read_b128 v[6:9], v102 offset:0
	ds_read_b128 v[10:13], v102 offset:0x800
	ds_read_b128 v[14:17], v102 offset:0x1000
	ds_read_b128 v[18:21], v102 offset:0x1800
	ds_read_b128 v[34:37], v110 offset:0
	ds_read_b128 v[38:41], v110 offset:0x800
	ds_read_b128 v[42:45], v110 offset:0x1000
	s_add_u32 s0, s0, s2
	s_addc_u32 s1, s1, 0
	s_lshl_b32 s2, s16, 10
	s_waitcnt lgkmcnt(2)
	s_add_u32 s2, s8, s2
	v_mfma_f32_16x16x32_bf16 v[46:49], v[6:9], v[34:37], v[94:97]
	s_addc_u32 s3, s9, 0
	v_mfma_f32_16x16x32_bf16 v[90:93], v[10:13], v[34:37], v[90:93]
	v_mfma_f32_16x16x32_bf16 v[86:89], v[14:17], v[34:37], v[86:89]
	v_mfma_f32_16x16x32_bf16 v[34:37], v[18:21], v[34:37], v[82:85]
	ds_read_b128 v[82:85], v110 offset:0x1800
	s_waitcnt lgkmcnt(2)
	v_mfma_f32_16x16x32_bf16 v[78:81], v[6:9], v[38:41], v[78:81]
	v_mfma_f32_16x16x32_bf16 v[74:77], v[10:13], v[38:41], v[74:77]
	v_mfma_f32_16x16x32_bf16 v[70:73], v[14:17], v[38:41], v[70:73]
	v_mfma_f32_16x16x32_bf16 v[38:41], v[18:21], v[38:41], v[66:69]
	s_waitcnt lgkmcnt(1)
	v_mfma_f32_16x16x32_bf16 v[62:65], v[6:9], v[42:45], v[62:65]
	v_mfma_f32_16x16x32_bf16 v[58:61], v[10:13], v[42:45], v[58:61]
	v_mfma_f32_16x16x32_bf16 v[54:57], v[14:17], v[42:45], v[54:57]
	v_mfma_f32_16x16x32_bf16 v[42:45], v[18:21], v[42:45], v[50:53]
	s_waitcnt lgkmcnt(0)
	v_mfma_f32_16x16x32_bf16 v[50:53], v[6:9], v[82:85], v[22:25]
	v_mfma_f32_16x16x32_bf16 v[66:69], v[10:13], v[82:85], v[26:29]
	v_mfma_f32_16x16x32_bf16 v[94:97], v[14:17], v[82:85], v[30:33]
	v_mfma_f32_16x16x32_bf16 v[2:5], v[18:21], v[82:85], v[2:5]
	ds_read_b128 v[18:21], v102 offset:0x400
	ds_read_b128 v[82:85], v102 offset:0xc00
	ds_read_b128 v[98:101], v102 offset:0x1400
	ds_read_b128 v[102:105], v102 offset:0x1c00
	ds_read_b128 v[6:9], v110 offset:0x400
	ds_read_b128 v[10:13], v110 offset:0xc00
	ds_read_b128 v[106:109], v110 offset:0x1400
	s_waitcnt lgkmcnt(2)
	v_mfma_f32_16x16x32_bf16 v[46:49], v[18:21], v[6:9], v[46:49]
	v_mfma_f32_16x16x32_bf16 v[90:93], v[82:85], v[6:9], v[90:93]
	v_mfma_f32_16x16x32_bf16 v[30:33], v[98:101], v[6:9], v[86:89]
	v_mfma_f32_16x16x32_bf16 v[14:17], v[102:105], v[6:9], v[34:37]
	ds_read_b128 v[86:89], v110 offset:0x1c00
	s_waitcnt lgkmcnt(2)
	v_mfma_f32_16x16x32_bf16 v[78:81], v[18:21], v[10:13], v[78:81]
	v_mfma_f32_16x16x32_bf16 v[74:77], v[82:85], v[10:13], v[74:77]
	v_mfma_f32_16x16x32_bf16 v[26:29], v[98:101], v[10:13], v[70:73]
	v_mfma_f32_16x16x32_bf16 v[10:13], v[102:105], v[10:13], v[38:41]
	s_waitcnt lgkmcnt(1)
	v_mfma_f32_16x16x32_bf16 v[62:65], v[18:21], v[106:109], v[62:65]
	v_mfma_f32_16x16x32_bf16 v[38:41], v[82:85], v[106:109], v[58:61]
	v_mfma_f32_16x16x32_bf16 v[22:25], v[98:101], v[106:109], v[54:57]
	v_mfma_f32_16x16x32_bf16 v[6:9], v[102:105], v[106:109], v[42:45]
	s_waitcnt lgkmcnt(0)
	v_mfma_f32_16x16x32_bf16 v[42:45], v[18:21], v[86:89], v[50:53]
	v_mfma_f32_16x16x32_bf16 v[34:37], v[82:85], v[86:89], v[66:69]
	v_mfma_f32_16x16x32_bf16 v[18:21], v[98:101], v[86:89], v[94:97]
	v_mfma_f32_16x16x32_bf16 v[2:5], v[102:105], v[86:89], v[2:5]
	v_lshrrev_b32_e32 v50, 2, v119
	v_and_b32_e32 v50, 12, v50
	v_lshl_or_b32 v66, v121, 6, v50
	v_lshlrev_b32_e32 v67, 2, v66
	s_waitcnt lgkmcnt(0)
	s_barrier
	global_load_dwordx4 v[50:53], v67, s[2:3]
	global_load_dwordx4 v[54:57], v67, s[2:3] offset:64
	v_lshrrev_b32_e32 v58, 1, v119
	v_lshl_or_b32 v59, v120, 6, v118
	v_and_b32_e32 v68, 8, v58
	v_lshl_add_u32 v69, v59, 9, 0
	v_or_b32_e32 v70, 16, v59
	v_or_b32_e32 v71, 48, v59
	v_lshrrev_b32_e32 v58, 3, v66
	v_or_b32_e32 v59, 16, v66
	v_bitop3_b32 v83, v70, v58, 31 bitop3:0x6c
	v_lshrrev_b32_e32 v85, 3, v59
	v_lshl_add_u32 v72, v70, 9, 0
	v_xor_b32_e32 v82, v58, v118
	v_bitop3_b32 v84, v71, v58, 31 bitop3:0x6c
	v_lshlrev_b32_e32 v83, 4, v83
	v_xor_b32_e32 v86, v85, v118
	v_lshl_add_u32 v73, v71, 9, 0
	v_lshlrev_b32_e32 v82, 4, v82
	v_lshlrev_b32_e32 v84, 4, v84
	v_add3_u32 v83, v72, v83, v68
	v_lshlrev_b32_e32 v86, 4, v86
	global_load_dwordx4 v[58:61], v67, s[2:3] offset:128
	v_add3_u32 v82, v69, v82, v68
	v_add3_u32 v84, v73, v84, v68
	v_add3_u32 v86, v69, v86, v68
	s_waitcnt vmcnt(2)
	v_add_f32_e32 v46, v46, v50
	v_add_f32_e32 v47, v47, v51
	v_add_f32_e32 v48, v48, v52
	v_add_f32_e32 v49, v49, v53
	v_add_f32_e32 v78, v78, v50
	v_add_f32_e32 v79, v79, v51
	v_add_f32_e32 v80, v80, v52
	v_add_f32_e32 v81, v81, v53
	v_add_f32_e32 v62, v62, v50
	v_add_f32_e32 v63, v63, v51
	v_add_f32_e32 v42, v42, v50
	v_add_f32_e32 v43, v43, v51
	v_add_f32_e32 v44, v44, v52
	v_add_f32_e32 v45, v45, v53
	s_waitcnt vmcnt(1)
	v_add_f32_e32 v50, v90, v54
	v_add_f32_e32 v51, v91, v55
	v_add_f32_e32 v64, v64, v52
	v_add_f32_e32 v65, v65, v53
	v_add_f32_e32 v52, v92, v56
	v_add_f32_e32 v53, v93, v57
	v_max_f32_e32 v46, 0, v46
	v_max_f32_e32 v47, 0, v47
	v_max_f32_e32 v48, 0, v48
	v_max_f32_e32 v49, 0, v49
	v_max_f32_e32 v78, 0, v78
	v_max_f32_e32 v79, 0, v79
	v_max_f32_e32 v80, 0, v80
	v_max_f32_e32 v81, 0, v81
	v_max_f32_e32 v88, 0, v43
	v_max_f32_e32 v89, 0, v44
	v_max_f32_e32 v90, 0, v45
	v_max_f32_e32 v50, 0, v50
	v_max_f32_e32 v51, 0, v51
	v_cvt_pk_bf16_f32 v43, v48, v49
	v_cvt_pk_bf16_f32 v44, v78, v79
	v_cvt_pk_bf16_f32 v45, v80, v81
	v_max_f32_e32 v62, 0, v62
	v_max_f32_e32 v63, 0, v63
	v_max_f32_e32 v64, 0, v64
	v_max_f32_e32 v65, 0, v65
	v_max_f32_e32 v87, 0, v42
	v_max_f32_e32 v52, 0, v52
	v_max_f32_e32 v53, 0, v53
	v_cvt_pk_bf16_f32 v42, v46, v47
	v_cvt_pk_bf16_f32 v46, v62, v63
	v_cvt_pk_bf16_f32 v47, v64, v65
	v_cvt_pk_bf16_f32 v48, v87, v88
	v_cvt_pk_bf16_f32 v49, v89, v90
	v_cvt_pk_bf16_f32 v50, v50, v51
	v_cvt_pk_bf16_f32 v51, v52, v53
	ds_write_b64 v83, v[44:45]
	ds_write2st64_b64 v82, v[42:43], v[46:47] offset1:32
	ds_write_b64 v84, v[48:49]
	ds_write_b64 v86, v[50:51]
	v_add_f32_e32 v43, v76, v56
	v_add_f32_e32 v44, v77, v57
	v_max_f32_e32 v43, 0, v43
	v_max_f32_e32 v44, 0, v44
	v_add_f32_e32 v42, v75, v55
	v_cvt_pk_bf16_f32 v43, v43, v44
	v_bitop3_b32 v44, v85, v70, 31 bitop3:0x78
	v_add_f32_e32 v74, v74, v54
	v_max_f32_e32 v42, 0, v42
	v_lshlrev_b32_e32 v44, 4, v44
	v_max_f32_e32 v74, 0, v74
	v_cvt_pk_bf16_f32 v42, v74, v42
	v_add3_u32 v44, v72, v44, v68
	ds_write_b64 v44, v[42:43]
	global_load_dwordx4 v[42:45], v67, s[2:3] offset:192
	v_add_f32_e32 v34, v34, v54
	v_add_f32_e32 v35, v35, v55
	v_add_f32_e32 v36, v36, v56
	v_max_f32_e32 v34, 0, v34
	v_max_f32_e32 v35, 0, v35
	v_max_f32_e32 v36, 0, v36
	v_add_f32_e32 v37, v37, v57
	v_max_f32_e32 v37, 0, v37
	v_cvt_pk_bf16_f32 v34, v34, v35
	v_cvt_pk_bf16_f32 v35, v36, v37
	v_bitop3_b32 v36, v85, v71, 31 bitop3:0x78
	v_add_f32_e32 v38, v38, v54
	v_add_f32_e32 v39, v39, v55
	v_lshlrev_b32_e32 v36, 4, v36
	v_max_f32_e32 v38, 0, v38
	v_max_f32_e32 v39, 0, v39
	v_add_f32_e32 v40, v40, v56
	v_add_f32_e32 v41, v41, v57
	v_add3_u32 v36, v73, v36, v68
	v_max_f32_e32 v40, 0, v40
	v_max_f32_e32 v41, 0, v41
	v_cvt_pk_bf16_f32 v38, v38, v39
	v_cvt_pk_bf16_f32 v39, v40, v41
	ds_write_b64 v86, v[38:39] offset:16384
	ds_write_b64 v36, v[34:35]
	v_or_b32_e32 v34, 32, v66
	s_waitcnt vmcnt(1)
	v_add_f32_e32 v30, v30, v58
	v_add_f32_e32 v31, v31, v59
	v_add_f32_e32 v32, v32, v60
	v_add_f32_e32 v26, v26, v58
	v_add_f32_e32 v27, v27, v59
	v_add_f32_e32 v28, v28, v60
	v_add_f32_e32 v18, v18, v58
	v_add_f32_e32 v19, v19, v59
	v_add_f32_e32 v20, v20, v60
	v_lshrrev_b32_e32 v34, 3, v34
	v_max_f32_e32 v30, 0, v30
	v_max_f32_e32 v31, 0, v31
	v_max_f32_e32 v32, 0, v32
	v_add_f32_e32 v33, v33, v61
	v_max_f32_e32 v26, 0, v26
	v_max_f32_e32 v27, 0, v27
	v_max_f32_e32 v28, 0, v28
	v_add_f32_e32 v29, v29, v61
	v_max_f32_e32 v18, 0, v18
	v_max_f32_e32 v19, 0, v19
	v_max_f32_e32 v20, 0, v20
	v_add_f32_e32 v21, v21, v61
	v_max_f32_e32 v33, 0, v33
	v_cvt_pk_bf16_f32 v30, v30, v31
	v_cvt_pk_bf16_f32 v31, v32, v33
	v_xor_b32_e32 v32, v34, v118
	v_max_f32_e32 v29, 0, v29
	v_cvt_pk_bf16_f32 v26, v26, v27
	v_cvt_pk_bf16_f32 v27, v28, v29
	v_bitop3_b32 v28, v34, v70, 31 bitop3:0x78
	v_max_f32_e32 v21, 0, v21
	v_cvt_pk_bf16_f32 v18, v18, v19
	v_cvt_pk_bf16_f32 v19, v20, v21
	v_bitop3_b32 v20, v34, v71, 31 bitop3:0x78
	v_lshlrev_b32_e32 v32, 4, v32
	v_lshlrev_b32_e32 v28, 4, v28
	v_add_f32_e32 v22, v22, v58
	v_add_f32_e32 v23, v23, v59
	v_lshlrev_b32_e32 v20, 4, v20
	v_add3_u32 v32, v69, v32, v68
	v_add3_u32 v28, v72, v28, v68
	v_max_f32_e32 v22, 0, v22
	v_max_f32_e32 v23, 0, v23
	v_add_f32_e32 v24, v24, v60
	v_add_f32_e32 v25, v25, v61
	v_add3_u32 v20, v73, v20, v68
	ds_write_b64 v32, v[30:31]
	ds_write_b64 v28, v[26:27]
	v_max_f32_e32 v24, 0, v24
	v_max_f32_e32 v25, 0, v25
	v_cvt_pk_bf16_f32 v22, v22, v23
	v_cvt_pk_bf16_f32 v23, v24, v25
	ds_write_b64 v32, v[22:23] offset:16384
	ds_write_b64 v20, v[18:19]
	v_or_b32_e32 v18, 48, v66
	s_waitcnt vmcnt(0)
	v_add_f32_e32 v14, v14, v42
	v_add_f32_e32 v15, v15, v43
	v_add_f32_e32 v16, v16, v44
	v_add_f32_e32 v10, v10, v42
	v_add_f32_e32 v11, v11, v43
	v_add_f32_e32 v12, v12, v44
	v_add_f32_e32 v2, v2, v42
	v_add_f32_e32 v3, v3, v43
	v_add_f32_e32 v4, v4, v44
	v_lshrrev_b32_e32 v18, 3, v18
	v_max_f32_e32 v14, 0, v14
	v_max_f32_e32 v15, 0, v15
	v_max_f32_e32 v16, 0, v16
	v_add_f32_e32 v17, v17, v45
	v_max_f32_e32 v10, 0, v10
	v_max_f32_e32 v11, 0, v11
	v_max_f32_e32 v12, 0, v12
	v_add_f32_e32 v13, v13, v45
	v_max_f32_e32 v2, 0, v2
	v_max_f32_e32 v3, 0, v3
	v_max_f32_e32 v4, 0, v4
	v_add_f32_e32 v5, v5, v45
	v_max_f32_e32 v17, 0, v17
	v_cvt_pk_bf16_f32 v14, v14, v15
	v_cvt_pk_bf16_f32 v15, v16, v17
	v_xor_b32_e32 v16, v18, v118
	v_max_f32_e32 v13, 0, v13
	v_cvt_pk_bf16_f32 v10, v10, v11
	v_cvt_pk_bf16_f32 v11, v12, v13
	v_bitop3_b32 v12, v18, v70, 31 bitop3:0x78
	v_max_f32_e32 v5, 0, v5
	v_cvt_pk_bf16_f32 v2, v2, v3
	v_cvt_pk_bf16_f32 v3, v4, v5
	v_bitop3_b32 v4, v18, v71, 31 bitop3:0x78
	v_lshlrev_b32_e32 v16, 4, v16
	v_lshlrev_b32_e32 v12, 4, v12
	v_add_f32_e32 v6, v6, v42
	v_add_f32_e32 v7, v7, v43
	v_lshlrev_b32_e32 v4, 4, v4
	v_add3_u32 v16, v69, v16, v68
	v_add3_u32 v12, v72, v12, v68
	v_max_f32_e32 v6, 0, v6
	v_max_f32_e32 v7, 0, v7
	v_add_f32_e32 v8, v8, v44
	v_add_f32_e32 v9, v9, v45
	v_add3_u32 v4, v73, v4, v68
	ds_write_b64 v16, v[14:15]
	ds_write_b64 v12, v[10:11]
	v_max_f32_e32 v8, 0, v8
	v_max_f32_e32 v9, 0, v9
	v_cvt_pk_bf16_f32 v6, v6, v7
	v_cvt_pk_bf16_f32 v7, v8, v9
	ds_write_b64 v16, v[6:7] offset:16384
	ds_write_b64 v4, v[2:3]
	v_and_b32_e32 v2, 0x1f0, v1
	v_mov_b32_e32 v3, 0
	v_lshl_add_u64 v[2:3], s[0:1], 0, v[2:3]
	s_mov_b64 s[0:1], 0x2000000
	v_ashrrev_i32_e32 v6, 5, v0
	v_lshl_add_u64 v[10:11], v[2:3], 0, s[0:1]
	v_xor_b32_e32 v2, v6, v0
	v_lshlrev_b32_e32 v2, 4, v2
	v_lshlrev_b32_e32 v1, 9, v6
	v_and_b32_e32 v2, 0x1f0, v2
	v_add3_u32 v1, 0, v1, v2
	s_waitcnt lgkmcnt(0)
	s_barrier
	ds_read_b128 v[2:5], v1
	v_ashrrev_i32_e32 v7, 31, v6
	v_add_u32_e32 v1, 0x200, v0
	v_lshlrev_b64 v[6:7], 11, v[6:7]
	v_ashrrev_i32_e32 v14, 5, v1
	v_lshl_add_u64 v[12:13], v[10:11], 0, v[6:7]
	v_xor_b32_e32 v6, v14, v0
	v_lshlrev_b32_e32 v6, 4, v6
	v_lshlrev_b32_e32 v1, 9, v14
	v_and_b32_e32 v6, 0x1f0, v6
	v_add3_u32 v1, 0, v1, v6
	ds_read_b128 v[6:9], v1
	v_ashrrev_i32_e32 v15, 31, v14
	s_waitcnt lgkmcnt(1)
	global_store_dwordx4 v[12:13], v[2:5], off sc1
	v_add_u32_e32 v1, 0x400, v0
	s_nop 0
	v_lshlrev_b64 v[2:3], 11, v[14:15]
	v_lshl_add_u64 v[2:3], v[10:11], 0, v[2:3]
	s_waitcnt lgkmcnt(0)
	global_store_dwordx4 v[2:3], v[6:9], off sc1
	s_nop 1
	v_ashrrev_i32_e32 v6, 5, v1
	v_xor_b32_e32 v2, v6, v0
	v_lshlrev_b32_e32 v2, 4, v2
	v_lshlrev_b32_e32 v1, 9, v6
	v_and_b32_e32 v2, 0x1f0, v2
	v_add3_u32 v1, 0, v1, v2
	ds_read_b128 v[2:5], v1
	v_ashrrev_i32_e32 v7, 31, v6
	v_add_u32_e32 v1, 0x600, v0
	v_lshlrev_b64 v[6:7], 11, v[6:7]
	v_ashrrev_i32_e32 v14, 5, v1
	v_lshl_add_u64 v[12:13], v[10:11], 0, v[6:7]
	v_xor_b32_e32 v6, v14, v0
	v_lshlrev_b32_e32 v6, 4, v6
	v_lshlrev_b32_e32 v1, 9, v14
	v_and_b32_e32 v6, 0x1f0, v6
	v_add3_u32 v1, 0, v1, v6
	ds_read_b128 v[6:9], v1
	v_ashrrev_i32_e32 v15, 31, v14
	s_waitcnt lgkmcnt(1)
	global_store_dwordx4 v[12:13], v[2:5], off sc1
	v_add_u32_e32 v1, 0x800, v0
	s_nop 0
	v_lshlrev_b64 v[2:3], 11, v[14:15]
	v_lshl_add_u64 v[2:3], v[10:11], 0, v[2:3]
	s_waitcnt lgkmcnt(0)
	global_store_dwordx4 v[2:3], v[6:9], off sc1
	s_nop 1
	v_ashrrev_i32_e32 v6, 5, v1
	v_xor_b32_e32 v2, v6, v0
	v_lshlrev_b32_e32 v2, 4, v2
	v_lshlrev_b32_e32 v1, 9, v6
	v_and_b32_e32 v2, 0x1f0, v2
	v_add3_u32 v1, 0, v1, v2
	ds_read_b128 v[2:5], v1
	v_ashrrev_i32_e32 v7, 31, v6
	v_add_u32_e32 v1, 0xa00, v0
	v_lshlrev_b64 v[6:7], 11, v[6:7]
	v_ashrrev_i32_e32 v14, 5, v1
	v_lshl_add_u64 v[12:13], v[10:11], 0, v[6:7]
	v_xor_b32_e32 v6, v14, v0
	v_lshlrev_b32_e32 v6, 4, v6
	v_lshlrev_b32_e32 v1, 9, v14
	v_and_b32_e32 v6, 0x1f0, v6
	v_add3_u32 v1, 0, v1, v6
	ds_read_b128 v[6:9], v1
	v_ashrrev_i32_e32 v15, 31, v14
	s_waitcnt lgkmcnt(1)
	global_store_dwordx4 v[12:13], v[2:5], off sc1
	v_add_u32_e32 v1, 0xc00, v0
	s_nop 0
	v_lshlrev_b64 v[2:3], 11, v[14:15]
	v_lshl_add_u64 v[2:3], v[10:11], 0, v[2:3]
	s_waitcnt lgkmcnt(0)
	global_store_dwordx4 v[2:3], v[6:9], off sc1
	s_nop 1
	v_ashrrev_i32_e32 v6, 5, v1
	v_xor_b32_e32 v2, v6, v0
	v_lshlrev_b32_e32 v2, 4, v2
	v_lshlrev_b32_e32 v1, 9, v6
	v_and_b32_e32 v2, 0x1f0, v2
	v_add3_u32 v1, 0, v1, v2
	ds_read_b128 v[2:5], v1
	v_add_u32_e32 v1, 0xe00, v0
	v_ashrrev_i32_e32 v14, 5, v1
	v_xor_b32_e32 v0, v14, v0
	v_lshlrev_b32_e32 v0, 4, v0
	v_ashrrev_i32_e32 v7, 31, v6
	v_lshlrev_b32_e32 v1, 9, v14
	v_and_b32_e32 v0, 0x1f0, v0
	v_lshlrev_b64 v[6:7], 11, v[6:7]
	v_add3_u32 v0, 0, v1, v0
	v_lshl_add_u64 v[12:13], v[10:11], 0, v[6:7]
	ds_read_b128 v[6:9], v0
	v_ashrrev_i32_e32 v15, 31, v14
	v_lshlrev_b64 v[0:1], 11, v[14:15]
	v_lshl_add_u64 v[0:1], v[10:11], 0, v[0:1]
	s_waitcnt lgkmcnt(1)
	global_store_dwordx4 v[12:13], v[2:5], off sc1
	s_waitcnt lgkmcnt(0)
	global_store_dwordx4 v[0:1], v[6:9], off sc1
	s_endpgm
